# EpiResid (P5/P8/P14/P17): second-half (ai=1) residual tile loads hoisted to the epilogue start into phase-free VGPRs v218-249, single vmcnt(8) wait instead of the 8-step ladder after the stores
# baseline (speedup 1.0000x reference)
;     __device__ __forceinline__ void operator()(const f32x4 (&acc)[2][2][4][2], const Unit& u, int wr, int wc, int fr, int fq) const {
;     ...
;             if (RES_BF16) {
; #pragma unroll
;                 for (int m = 0; m < 4; ++m)
; #pragma unroll
;                     for (int bj = 0; bj < 2; ++bj)
;                         rw[m][bj] = *(const u32x4*)(xb + (size_t)(u.pm * BM + ai * HALF + wr * 64 + m * 16 + fr) * 1024 + u.pn * BM + bj * HALF + wc * 32 + 8 * fq);
; #pragma unroll
;                 for (int m = 0; m < 4; ++m)
; #pragma unroll
;                     for (int bj = 0; bj < 2; ++bj) asm volatile("" : "+v"(rw[m][bj]));
;             }
; #pragma unroll
;             for (int m = 0; m < 4; ++m) {
;                 const int row = u.pm * BM + ai * HALF + wr * 64 + m * 16 + fr;
;                 float s = 0.f;
; #pragma unroll
;                 for (int bj = 0; bj < 2; ++bj) {
;                     const size_t off = (size_t)row * 1024 + u.pn * BM + bj * HALF + wc * 32 + 8 * fq;
;                     f32x4 r0, r1;
;                     if (RES_BF16) {
;                         const u32x4 w_ = rw[m][bj];
;                         r0 = (f32x4){__uint_as_float(w_.x << 16), __uint_as_float(w_.x & 0xffff0000u), __uint_as_float(w_.y << 16), __uint_as_float(w_.y & 0xffff0000u)};
;                         r1 = (f32x4){__uint_as_float(w_.z << 16), __uint_as_float(w_.z & 0xffff0000u), __uint_as_float(w_.w << 16), __uint_as_float(w_.w & 0xffff0000u)};
;                     } else { r0 = *(const f32x4*)(resid + off); r1 = *(const f32x4*)(resid + off + 4); }
;                     f32x4 v0, v1;
; #pragma unroll
;                     for (int j = 0; j < 4; ++j) { v0[j] = acc[ai][bj][m][0][j] + r0[j]; v1[j] = acc[ai][bj][m][1][j] + r1[j]; }
;                     if (OUT_F32) { *(f32x4*)(xout + off) = v0; *(f32x4*)(xout + off + 4) = v1; }
;                     else {
;                         u32x4 w; w.x = cvt_pk_bf16(v0[0], v0[1]); w.y = cvt_pk_bf16(v0[2], v0[3]); w.z = cvt_pk_bf16(v1[0], v1[1]); w.w = cvt_pk_bf16(v1[2], v1[3]);
;                         *(u32x4*)(xb + off) = w;
;                     }
;                     s += dot4(v0) + dot4(v1);
;                 }
;                 s += __shfl_xor(s, 16); s += __shfl_xor(s, 32);
;                 if (fq == 0) ssq[(size_t)row * 16 + u.pn * 4 + wc] = s;
.LBB0_1783:
	v_lshl_add_u32 v172, s28, 8, v188
	s_lshl_b32 s28, s26, 8
	s_ashr_i32 s29, s28, 31
	s_lshl_b64 s[30:31], s[28:29], 1
	v_ashrrev_i32_e32 v173, 31, v172
	v_lshl_add_u64 v[174:175], v[162:163], 0, s[30:31]
	v_lshlrev_b64 v[202:203], 11, v[172:173]
	v_lshl_add_u64 v[128:129], v[174:175], 0, v[202:203]
	v_or_b32_e32 v184, 16, v172
	global_load_dwordx4 v[194:197], v[128:129], off
	global_load_dwordx4 v[198:201], v[128:129], off offset:256
	v_ashrrev_i32_e32 v185, 31, v184
	v_or_b32_e32 v180, 32, v172
	v_lshlrev_b64 v[186:187], 11, v[184:185]
	v_ashrrev_i32_e32 v181, 31, v180
	v_or_b32_e32 v176, 48, v172
	v_lshl_add_u64 v[128:129], v[174:175], 0, v[186:187]
	v_lshlrev_b64 v[182:183], 11, v[180:181]
	v_ashrrev_i32_e32 v177, 31, v176
	global_load_dwordx4 v[148:151], v[128:129], off
	global_load_dwordx4 v[144:147], v[128:129], off offset:256
	v_lshl_add_u64 v[128:129], v[174:175], 0, v[182:183]
	v_lshlrev_b64 v[178:179], 11, v[176:177]
	global_load_dwordx4 v[140:143], v[128:129], off
	global_load_dwordx4 v[136:139], v[128:129], off offset:256
	v_lshl_add_u64 v[128:129], v[174:175], 0, v[178:179]
	global_load_dwordx4 v[132:135], v[128:129], off
	s_nop 0
	global_load_dwordx4 v[128:131], v[128:129], off offset:256
	v_add_u32_e32 v250, 0x80, v172
	v_ashrrev_i32_e32 v251, 31, v250
	v_lshlrev_b64 v[250:251], 11, v[250:251]
	v_lshl_add_u64 v[250:251], v[174:175], 0, v[250:251]
	global_load_dwordx4 v[218:221], v[250:251], off
	global_load_dwordx4 v[222:225], v[250:251], off offset:256
	v_add_u32_e32 v250, 0x90, v172
	v_ashrrev_i32_e32 v251, 31, v250
	v_lshlrev_b64 v[250:251], 11, v[250:251]
	v_lshl_add_u64 v[250:251], v[174:175], 0, v[250:251]
	global_load_dwordx4 v[226:229], v[250:251], off
	global_load_dwordx4 v[230:233], v[250:251], off offset:256
	v_add_u32_e32 v250, 0xa0, v172
	v_ashrrev_i32_e32 v251, 31, v250
	v_lshlrev_b64 v[250:251], 11, v[250:251]
	v_lshl_add_u64 v[250:251], v[174:175], 0, v[250:251]
	global_load_dwordx4 v[234:237], v[250:251], off
	global_load_dwordx4 v[238:241], v[250:251], off offset:256
	v_add_u32_e32 v250, 0xb0, v172
	v_ashrrev_i32_e32 v251, 31, v250
	v_lshlrev_b64 v[250:251], 11, v[250:251]
	v_lshl_add_u64 v[250:251], v[174:175], 0, v[250:251]
	global_load_dwordx4 v[242:245], v[250:251], off
	global_load_dwordx4 v[246:249], v[250:251], off offset:256
	v_lshl_add_u64 v[202:203], s[10:11], 0, v[202:203]
	v_lshl_add_u64 v[202:203], v[202:203], 0, s[30:31]
	s_lshl_b32 s26, s26, 2
	s_ashr_i32 s27, s26, 31
	s_waitcnt vmcnt(8)
	s_nop 0
	v_lshlrev_b32_e32 v204, 16, v194
	v_and_b32_e32 v194, 0xffff0000, v194
	v_lshlrev_b32_e32 v205, 16, v195
	v_and_b32_e32 v195, 0xffff0000, v195
	v_lshlrev_b32_e32 v206, 16, v196
	v_and_b32_e32 v196, 0xffff0000, v196
	v_lshlrev_b32_e32 v207, 16, v197
	v_and_b32_e32 v197, 0xffff0000, v197
	v_lshlrev_b32_e32 v208, 16, v198
	v_and_b32_e32 v198, 0xffff0000, v198
	v_lshlrev_b32_e32 v209, 16, v199
	v_and_b32_e32 v199, 0xffff0000, v199
	v_lshlrev_b32_e32 v210, 16, v200
	v_and_b32_e32 v200, 0xffff0000, v200
	v_add_f32_e32 v125, v125, v194
	v_add_f32_e32 v121, v121, v196
	v_add_f32_e32 v127, v127, v195
	v_add_f32_e32 v123, v123, v197
	v_add_f32_e32 v124, v124, v204
	v_add_f32_e32 v120, v120, v206
	v_add_f32_e32 v126, v126, v205
	v_add_f32_e32 v122, v122, v207
	v_add_f32_e32 v195, v112, v210
	v_add_f32_e32 v196, v117, v198
	v_add_f32_e32 v197, v113, v200
	v_add_f32_e32 v198, v118, v209
	v_add_f32_e32 v199, v119, v199
	v_mul_f32_e32 v112, v125, v125
	v_mul_f32_e32 v113, v127, v127
	v_mul_f32_e32 v118, v121, v121
	v_mul_f32_e32 v119, v123, v123
	v_lshlrev_b32_e32 v211, 16, v201
	v_and_b32_e32 v201, 0xffff0000, v201
	v_fmac_f32_e32 v112, v124, v124
	v_fmac_f32_e32 v113, v126, v126
	v_fmac_f32_e32 v118, v120, v120
	v_fmac_f32_e32 v119, v122, v122
	v_add_f32_e32 v201, v115, v201
	v_add_f32_e32 v112, v112, v113
	v_add_f32_e32 v113, v118, v119
	v_add_f32_e32 v194, v116, v208
	v_add_f32_e32 v200, v114, v211
	v_cvt_pk_bf16_f32 v114, v124, v125
	v_cvt_pk_bf16_f32 v115, v126, v127
	v_cvt_pk_bf16_f32 v116, v120, v121
	v_cvt_pk_bf16_f32 v117, v122, v123
	v_mul_f32_e32 v121, v196, v196
	v_mul_f32_e32 v123, v199, v199
	v_add_f32_e32 v112, v112, v113
	v_mul_f32_e32 v113, v197, v197
	v_mul_f32_e32 v119, v201, v201
	v_fmac_f32_e32 v121, v194, v194
	v_fmac_f32_e32 v123, v198, v198
	v_fmac_f32_e32 v113, v195, v195
	v_fmac_f32_e32 v119, v200, v200
	v_add_f32_e32 v118, v121, v123
	v_add_f32_e32 v113, v113, v119
	v_add_f32_e32 v113, v118, v113
	v_and_b32_e32 v118, 64, v193
	v_add_f32_e32 v113, v112, v113
	v_xor_b32_e32 v112, 16, v193
	v_add_u32_e32 v122, 64, v118
	v_cmp_lt_i32_e32 vcc, v112, v122
	v_lshl_add_u64 v[118:119], v[202:203], 0, s[6:7]
	v_lshl_add_u64 v[120:121], v[118:119], 0, v[160:161]
	v_cndmask_b32_e32 v112, v193, v112, vcc
	v_lshlrev_b32_e32 v112, 2, v112
	ds_bpermute_b32 v123, v112, v113
	global_store_dwordx4 v[120:121], v[114:117], off
	s_nop 1
	v_cvt_pk_bf16_f32 v116, v194, v196
	s_waitcnt lgkmcnt(0)
	v_add_f32_e32 v114, v113, v123
	v_xor_b32_e32 v113, 32, v193
	v_cmp_lt_i32_e32 vcc, v113, v122
	v_cvt_pk_bf16_f32 v117, v198, v199
	v_cvt_pk_bf16_f32 v118, v195, v197
	v_cvt_pk_bf16_f32 v119, v200, v201
	global_store_dwordx4 v[120:121], v[116:119], off offset:256
	s_nop 0
	v_cndmask_b32_e32 v113, v193, v113, vcc
	v_lshlrev_b32_e32 v113, 2, v113
	ds_bpermute_b32 v115, v113, v114
	s_and_saveexec_b64 s[30:31], s[2:3]
	s_cbranch_execz .LBB0_1785
	v_lshlrev_b64 v[116:117], 6, v[172:173]
	v_lshl_add_u64 v[116:117], s[12:13], 0, v[116:117]
	v_lshl_add_u64 v[116:117], s[26:27], 2, v[116:117]
	s_lshl_b32 s34, s46, 2
	s_mov_b32 s35, s7
	v_lshl_add_u64 v[116:117], v[116:117], 0, s[34:35]
	s_waitcnt lgkmcnt(0)
	v_add_f32_e32 v114, v114, v115
	global_store_dword v[116:117], v114, off

; __device__ __forceinline__ unsigned cvt_pk_bf16(float lo, float hi) { unsigned r; asm volatile("v_cvt_pk_bf16_f32 %0, %1, %2" : "=v"(r) : "v"(lo), "v"(hi)); return r; }
; __device__ __forceinline__ float dot4(f32x4 v) { return (v.x * v.x + v.y * v.y) + (v.z * v.z + v.w * v.w); }
;     __device__ __forceinline__ void operator()(const f32x4 (&acc)[2][2][4][2], const Unit& u, int wr, int wc, int fr, int fq) const {
;     ...
;             for (int m = 0; m < 4; ++m) {
;                 const int row = u.pm * BM + ai * HALF + wr * 64 + m * 16 + fr;
;                 float s = 0.f;
; #pragma unroll
;                 for (int bj = 0; bj < 2; ++bj) {
;                     const size_t off = (size_t)row * 1024 + u.pn * BM + bj * HALF + wc * 32 + 8 * fq;
;                     f32x4 r0, r1;
;                     if (RES_BF16) {
;                         const u32x4 w_ = rw[m][bj];
;                         r0 = (f32x4){__uint_as_float(w_.x << 16), __uint_as_float(w_.x & 0xffff0000u), __uint_as_float(w_.y << 16), __uint_as_float(w_.y & 0xffff0000u)};
;                         r1 = (f32x4){__uint_as_float(w_.z << 16), __uint_as_float(w_.z & 0xffff0000u), __uint_as_float(w_.w << 16), __uint_as_float(w_.w & 0xffff0000u)};
;                     } else { r0 = *(const f32x4*)(resid + off); r1 = *(const f32x4*)(resid + off + 4); }
;                     f32x4 v0, v1;
; #pragma unroll
;                     for (int j = 0; j < 4; ++j) { v0[j] = acc[ai][bj][m][0][j] + r0[j]; v1[j] = acc[ai][bj][m][1][j] + r1[j]; }
;                     if (OUT_F32) { *(f32x4*)(xout + off) = v0; *(f32x4*)(xout + off + 4) = v1; }
;                     else {
;                         u32x4 w; w.x = cvt_pk_bf16(v0[0], v0[1]); w.y = cvt_pk_bf16(v0[2], v0[3]); w.z = cvt_pk_bf16(v1[0], v1[1]); w.w = cvt_pk_bf16(v1[2], v1[3]);
;                         *(u32x4*)(xb + off) = w;
;                     }
;                     s += dot4(v0) + dot4(v1);
;                 }
;                 s += __shfl_xor(s, 16); s += __shfl_xor(s, 32);
;                 if (fq == 0) ssq[(size_t)row * 16 + u.pn * 4 + wc] = s;
.LBB0_1791:
	s_or_b64 exec, exec, s[30:31]
	v_add_u32_e32 v100, 0x80, v172
	v_ashrrev_i32_e32 v101, 31, v100
	v_add_u32_e32 v96, 0x90, v172
	v_lshlrev_b64 v[110:111], 11, v[100:101]
	v_ashrrev_i32_e32 v97, 31, v96
	v_add_u32_e32 v92, 0xa0, v172
	s_waitcnt lgkmcnt(0)
	v_lshlrev_b64 v[98:99], 11, v[96:97]
	v_ashrrev_i32_e32 v93, 31, v92
	v_add_u32_e32 v88, 0xb0, v172
	v_lshlrev_b64 v[94:95], 11, v[92:93]
	v_ashrrev_i32_e32 v89, 31, v88
	v_lshlrev_b64 v[90:91], 11, v[88:89]
	v_lshl_add_u64 v[110:111], s[10:11], 0, v[110:111]
	v_lshl_add_u64 v[110:111], s[28:29], 1, v[110:111]
	s_waitcnt vmcnt(8)
	v_lshlrev_b32_e32 v114, 16, v218
	v_and_b32_e32 v102, 0xffff0000, v218
	v_lshlrev_b32_e32 v115, 16, v219
	v_and_b32_e32 v103, 0xffff0000, v219
	v_lshlrev_b32_e32 v116, 16, v220
	v_and_b32_e32 v104, 0xffff0000, v220
	v_lshlrev_b32_e32 v117, 16, v221
	v_and_b32_e32 v105, 0xffff0000, v221
	v_lshlrev_b32_e32 v118, 16, v222
	v_and_b32_e32 v106, 0xffff0000, v222
	v_lshlrev_b32_e32 v119, 16, v223
	v_and_b32_e32 v107, 0xffff0000, v223
	v_lshlrev_b32_e32 v120, 16, v224
	v_and_b32_e32 v108, 0xffff0000, v224
	v_lshlrev_b32_e32 v121, 16, v225
	v_and_b32_e32 v109, 0xffff0000, v225
	v_add_f32_e32 v61, v61, v102
	v_add_f32_e32 v57, v57, v104
	v_add_f32_e32 v63, v63, v103
	v_add_f32_e32 v59, v59, v105
	v_add_f32_e32 v104, v53, v106
	v_add_f32_e32 v105, v49, v108
	v_add_f32_e32 v107, v55, v107
	v_add_f32_e32 v109, v51, v109
	v_add_f32_e32 v60, v60, v114
	v_add_f32_e32 v56, v56, v116
	v_add_f32_e32 v62, v62, v115
	v_add_f32_e32 v58, v58, v117
	v_add_f32_e32 v102, v52, v118
	v_add_f32_e32 v103, v48, v120
	v_add_f32_e32 v106, v54, v119
	v_add_f32_e32 v108, v50, v121
	v_cvt_pk_bf16_f32 v48, v60, v61
	v_cvt_pk_bf16_f32 v49, v62, v63
	v_cvt_pk_bf16_f32 v50, v56, v57
	v_cvt_pk_bf16_f32 v51, v58, v59
	v_mul_f32_e32 v52, v61, v61
	v_mul_f32_e32 v53, v63, v63
	v_mul_f32_e32 v54, v57, v57
	v_mul_f32_e32 v55, v59, v59
	v_mul_f32_e32 v57, v104, v104
	v_mul_f32_e32 v59, v107, v107
	v_mul_f32_e32 v61, v105, v105
	v_mul_f32_e32 v63, v109, v109
	v_fmac_f32_e32 v52, v60, v60
	v_fmac_f32_e32 v53, v62, v62
	v_fmac_f32_e32 v54, v56, v56
	v_fmac_f32_e32 v55, v58, v58
	v_fmac_f32_e32 v57, v102, v102
	v_fmac_f32_e32 v59, v106, v106
	v_fmac_f32_e32 v61, v103, v103
	v_fmac_f32_e32 v63, v108, v108
	v_add_f32_e32 v52, v52, v53
	v_add_f32_e32 v53, v54, v55
	v_add_f32_e32 v54, v57, v59
	v_add_f32_e32 v55, v61, v63
	v_add_f32_e32 v52, v52, v53
	v_add_f32_e32 v53, v54, v55
	v_add_f32_e32 v56, v52, v53
	ds_bpermute_b32 v57, v112, v56
	v_lshl_add_u64 v[52:53], v[110:111], 0, s[6:7]
	v_lshl_add_u64 v[54:55], v[52:53], 0, v[160:161]
	global_store_dwordx4 v[54:55], v[48:51], off
	s_waitcnt lgkmcnt(0)
	s_nop 0
	v_add_f32_e32 v48, v56, v57
	ds_bpermute_b32 v49, v113, v48
	v_cvt_pk_bf16_f32 v50, v102, v104
	v_cvt_pk_bf16_f32 v51, v106, v107
	v_cvt_pk_bf16_f32 v52, v103, v105
	v_cvt_pk_bf16_f32 v53, v108, v109
	global_store_dwordx4 v[54:55], v[50:53], off offset:256
	s_and_saveexec_b64 s[30:31], s[2:3]
	s_cbranch_execz .LBB0_1793
	v_lshlrev_b64 v[50:51], 6, v[100:101]
	v_lshl_add_u64 v[50:51], s[12:13], 0, v[50:51]
	v_lshl_add_u64 v[50:51], s[26:27], 2, v[50:51]
	s_lshl_b32 s34, s46, 2
	s_mov_b32 s35, s7
	v_lshl_add_u64 v[50:51], v[50:51], 0, s[34:35]
	s_waitcnt lgkmcnt(0)
	v_add_f32_e32 v48, v48, v49
	global_store_dword v[50:51], v48, off
.LBB0_1793:
	s_or_b64 exec, exec, s[30:31]
	s_waitcnt lgkmcnt(0)
	v_and_b32_e32 v49, 0xffff0000, v226
	v_and_b32_e32 v51, 0xffff0000, v227
	v_lshlrev_b32_e32 v48, 16, v226
	v_lshlrev_b32_e32 v50, 16, v227
	v_lshlrev_b32_e32 v52, 16, v228
	v_and_b32_e32 v53, 0xffff0000, v228
	v_add_f32_e32 v49, v45, v49
	v_add_f32_e32 v47, v47, v51
	v_and_b32_e32 v55, 0xffff0000, v229
	v_add_f32_e32 v48, v44, v48
	v_add_f32_e32 v52, v40, v52
	v_add_f32_e32 v53, v41, v53
	v_add_f32_e32 v46, v46, v50
	v_cvt_pk_bf16_f32 v40, v48, v49
	v_cvt_pk_bf16_f32 v41, v46, v47
	v_mul_f32_e32 v49, v49, v49
	v_mul_f32_e32 v47, v47, v47
	v_lshlrev_b32_e32 v54, 16, v229
	v_add_f32_e32 v51, v43, v55
	v_fmac_f32_e32 v49, v48, v48
	v_fmac_f32_e32 v47, v46, v46
	v_add_f32_e32 v50, v42, v54
	v_add_f32_e32 v46, v49, v47
	v_mul_f32_e32 v47, v53, v53
	v_mul_f32_e32 v48, v51, v51
	v_fmac_f32_e32 v47, v52, v52
	v_fmac_f32_e32 v48, v50, v50
	v_cvt_pk_bf16_f32 v42, v52, v53
	v_cvt_pk_bf16_f32 v43, v50, v51
	v_add_f32_e32 v47, v47, v48
	v_and_b32_e32 v48, 0xffff0000, v230
	v_and_b32_e32 v50, 0xffff0000, v231
	v_add_f32_e32 v46, v46, v47
	v_lshlrev_b32_e32 v47, 16, v230
	v_lshlrev_b32_e32 v49, 16, v231
	v_lshlrev_b32_e32 v51, 16, v232
	v_and_b32_e32 v52, 0xffff0000, v232
	v_add_f32_e32 v37, v37, v48
	v_add_f32_e32 v50, v39, v50
	v_and_b32_e32 v54, 0xffff0000, v233
	v_add_f32_e32 v36, v36, v47
	v_add_f32_e32 v47, v32, v51
	v_add_f32_e32 v48, v33, v52
	v_add_f32_e32 v49, v38, v49
	v_mul_f32_e32 v32, v37, v37
	v_mul_f32_e32 v33, v50, v50
	v_lshlrev_b32_e32 v53, 16, v233
	v_add_f32_e32 v52, v35, v54
	v_fmac_f32_e32 v32, v36, v36
	v_fmac_f32_e32 v33, v49, v49
	v_add_f32_e32 v51, v34, v53
	v_add_f32_e32 v32, v32, v33
	v_mul_f32_e32 v33, v48, v48
	v_mul_f32_e32 v34, v52, v52
	v_fmac_f32_e32 v33, v47, v47
	v_fmac_f32_e32 v34, v51, v51
	v_add_f32_e32 v33, v33, v34
	v_add_f32_e32 v32, v32, v33
	v_add_f32_e32 v35, v46, v32
	ds_bpermute_b32 v46, v112, v35
	v_lshl_add_u64 v[44:45], s[10:11], 0, v[98:99]
	v_lshl_add_u64 v[44:45], s[28:29], 1, v[44:45]
	v_lshl_add_u64 v[32:33], v[44:45], 0, s[6:7]
	v_lshl_add_u64 v[38:39], v[32:33], 0, v[160:161]
	s_waitcnt lgkmcnt(0)
	v_add_f32_e32 v32, v35, v46
	ds_bpermute_b32 v33, v113, v32
	global_store_dwordx4 v[38:39], v[40:43], off
	v_cvt_pk_bf16_f32 v34, v36, v37
	v_cvt_pk_bf16_f32 v35, v49, v50
	v_cvt_pk_bf16_f32 v36, v47, v48
	v_cvt_pk_bf16_f32 v37, v51, v52
	global_store_dwordx4 v[38:39], v[34:37], off offset:256
	s_and_saveexec_b64 s[30:31], s[2:3]
	s_cbranch_execz .LBB0_1795
	v_lshlrev_b64 v[34:35], 6, v[96:97]
	v_lshl_add_u64 v[34:35], s[12:13], 0, v[34:35]
	v_lshl_add_u64 v[34:35], s[26:27], 2, v[34:35]
	s_lshl_b32 s34, s46, 2
	s_mov_b32 s35, s7
	v_lshl_add_u64 v[34:35], v[34:35], 0, s[34:35]
	s_waitcnt lgkmcnt(0)
	v_add_f32_e32 v32, v32, v33
	global_store_dword v[34:35], v32, off
; __device__ __forceinline__ unsigned cvt_pk_bf16(float lo, float hi) { unsigned r; asm volatile("v_cvt_pk_bf16_f32 %0, %1, %2" : "=v"(r) : "v"(lo), "v"(hi)); return r; }
; __device__ __forceinline__ float dot4(f32x4 v) { return (v.x * v.x + v.y * v.y) + (v.z * v.z + v.w * v.w); }
;     __device__ __forceinline__ void operator()(const f32x4 (&acc)[2][2][4][2], const Unit& u, int wr, int wc, int fr, int fq) const {
;     ...
;             for (int m = 0; m < 4; ++m) {
;                 const int row = u.pm * BM + ai * HALF + wr * 64 + m * 16 + fr;
;                 float s = 0.f;
; #pragma unroll
;                 for (int bj = 0; bj < 2; ++bj) {
;                     const size_t off = (size_t)row * 1024 + u.pn * BM + bj * HALF + wc * 32 + 8 * fq;
;                     f32x4 r0, r1;
;                     if (RES_BF16) {
;                         const u32x4 w_ = rw[m][bj];
;                         r0 = (f32x4){__uint_as_float(w_.x << 16), __uint_as_float(w_.x & 0xffff0000u), __uint_as_float(w_.y << 16), __uint_as_float(w_.y & 0xffff0000u)};
;                         r1 = (f32x4){__uint_as_float(w_.z << 16), __uint_as_float(w_.z & 0xffff0000u), __uint_as_float(w_.w << 16), __uint_as_float(w_.w & 0xffff0000u)};
;                     } else { r0 = *(const f32x4*)(resid + off); r1 = *(const f32x4*)(resid + off + 4); }
;                     f32x4 v0, v1;
; #pragma unroll
;                     for (int j = 0; j < 4; ++j) { v0[j] = acc[ai][bj][m][0][j] + r0[j]; v1[j] = acc[ai][bj][m][1][j] + r1[j]; }
;                     if (OUT_F32) { *(f32x4*)(xout + off) = v0; *(f32x4*)(xout + off + 4) = v1; }
;                     else {
;                         u32x4 w; w.x = cvt_pk_bf16(v0[0], v0[1]); w.y = cvt_pk_bf16(v0[2], v0[3]); w.z = cvt_pk_bf16(v1[0], v1[1]); w.w = cvt_pk_bf16(v1[2], v1[3]);
;                         *(u32x4*)(xb + off) = w;
;                     }
;                     s += dot4(v0) + dot4(v1);
;                 }
;                 s += __shfl_xor(s, 16); s += __shfl_xor(s, 32);
;                 if (fq == 0) ssq[(size_t)row * 16 + u.pn * 4 + wc] = s;
.LBB0_1795:
	s_or_b64 exec, exec, s[30:31]
	s_waitcnt lgkmcnt(0)
	v_and_b32_e32 v33, 0xffff0000, v234
	v_and_b32_e32 v35, 0xffff0000, v235
	v_lshlrev_b32_e32 v32, 16, v234
	v_lshlrev_b32_e32 v34, 16, v235
	v_lshlrev_b32_e32 v36, 16, v236
	v_and_b32_e32 v37, 0xffff0000, v236
	v_add_f32_e32 v33, v29, v33
	v_add_f32_e32 v31, v31, v35
	v_and_b32_e32 v39, 0xffff0000, v237
	v_add_f32_e32 v32, v28, v32
	v_add_f32_e32 v36, v24, v36
	v_add_f32_e32 v37, v25, v37
	v_add_f32_e32 v30, v30, v34
	v_cvt_pk_bf16_f32 v24, v32, v33
	v_cvt_pk_bf16_f32 v25, v30, v31
	v_mul_f32_e32 v33, v33, v33
	v_mul_f32_e32 v31, v31, v31
	v_lshlrev_b32_e32 v38, 16, v237
	v_add_f32_e32 v35, v27, v39
	v_fmac_f32_e32 v33, v32, v32
	v_fmac_f32_e32 v31, v30, v30
	v_add_f32_e32 v34, v26, v38
	v_add_f32_e32 v30, v33, v31
	v_mul_f32_e32 v31, v37, v37
	v_mul_f32_e32 v32, v35, v35
	v_fmac_f32_e32 v31, v36, v36
	v_fmac_f32_e32 v32, v34, v34
	v_cvt_pk_bf16_f32 v26, v36, v37
	v_cvt_pk_bf16_f32 v27, v34, v35
	v_add_f32_e32 v31, v31, v32
	v_and_b32_e32 v32, 0xffff0000, v238
	v_and_b32_e32 v34, 0xffff0000, v239
	v_add_f32_e32 v30, v30, v31
	v_lshlrev_b32_e32 v31, 16, v238
	v_lshlrev_b32_e32 v33, 16, v239
	v_lshlrev_b32_e32 v35, 16, v240
	v_and_b32_e32 v36, 0xffff0000, v240
	v_add_f32_e32 v21, v21, v32
	v_add_f32_e32 v34, v23, v34
	v_and_b32_e32 v38, 0xffff0000, v241
	v_add_f32_e32 v20, v20, v31
	v_add_f32_e32 v31, v16, v35
	v_add_f32_e32 v32, v17, v36
	v_add_f32_e32 v33, v22, v33
	v_mul_f32_e32 v16, v21, v21
	v_mul_f32_e32 v17, v34, v34
	v_lshlrev_b32_e32 v37, 16, v241
	v_add_f32_e32 v36, v19, v38
	v_fmac_f32_e32 v16, v20, v20
	v_fmac_f32_e32 v17, v33, v33
	v_add_f32_e32 v35, v18, v37
	v_add_f32_e32 v16, v16, v17
	v_mul_f32_e32 v17, v32, v32
	v_mul_f32_e32 v18, v36, v36
	v_fmac_f32_e32 v17, v31, v31
	v_fmac_f32_e32 v18, v35, v35
	v_add_f32_e32 v17, v17, v18
	v_add_f32_e32 v16, v16, v17
	v_add_f32_e32 v19, v30, v16
	ds_bpermute_b32 v30, v112, v19
	v_lshl_add_u64 v[28:29], s[10:11], 0, v[94:95]
	v_lshl_add_u64 v[28:29], s[28:29], 1, v[28:29]
	v_lshl_add_u64 v[16:17], v[28:29], 0, s[6:7]
	v_lshl_add_u64 v[22:23], v[16:17], 0, v[160:161]
	s_waitcnt lgkmcnt(0)
	v_add_f32_e32 v16, v19, v30
	ds_bpermute_b32 v17, v113, v16
	global_store_dwordx4 v[22:23], v[24:27], off
	v_cvt_pk_bf16_f32 v18, v20, v21
	v_cvt_pk_bf16_f32 v19, v33, v34
	v_cvt_pk_bf16_f32 v20, v31, v32
	v_cvt_pk_bf16_f32 v21, v35, v36
	global_store_dwordx4 v[22:23], v[18:21], off offset:256
	s_and_saveexec_b64 s[30:31], s[2:3]
	s_cbranch_execz .LBB0_1797
	v_lshlrev_b64 v[18:19], 6, v[92:93]
	v_lshl_add_u64 v[18:19], s[12:13], 0, v[18:19]
	v_lshl_add_u64 v[18:19], s[26:27], 2, v[18:19]
	s_lshl_b32 s34, s46, 2
	s_mov_b32 s35, s7
	v_lshl_add_u64 v[18:19], v[18:19], 0, s[34:35]
	s_waitcnt lgkmcnt(0)
	v_add_f32_e32 v16, v16, v17
	global_store_dword v[18:19], v16, off
.LBB0_1797:
	s_or_b64 exec, exec, s[30:31]
	s_waitcnt lgkmcnt(0)
	v_and_b32_e32 v17, 0xffff0000, v242
	v_and_b32_e32 v19, 0xffff0000, v243
	v_lshlrev_b32_e32 v16, 16, v242
	v_lshlrev_b32_e32 v18, 16, v243
	v_lshlrev_b32_e32 v20, 16, v244
	v_and_b32_e32 v21, 0xffff0000, v244
	v_add_f32_e32 v17, v13, v17
	v_add_f32_e32 v15, v15, v19
	v_and_b32_e32 v23, 0xffff0000, v245
	v_add_f32_e32 v16, v12, v16
	v_add_f32_e32 v20, v8, v20
	v_add_f32_e32 v21, v9, v21
	v_add_f32_e32 v14, v14, v18
	v_cvt_pk_bf16_f32 v8, v16, v17
	v_cvt_pk_bf16_f32 v9, v14, v15
	v_mul_f32_e32 v17, v17, v17
	v_mul_f32_e32 v15, v15, v15
	v_lshlrev_b32_e32 v22, 16, v245
	v_add_f32_e32 v19, v11, v23
	v_fmac_f32_e32 v17, v16, v16
	v_fmac_f32_e32 v15, v14, v14
	v_add_f32_e32 v18, v10, v22
	v_add_f32_e32 v14, v17, v15
	v_mul_f32_e32 v15, v21, v21
	v_mul_f32_e32 v16, v19, v19
	v_fmac_f32_e32 v15, v20, v20
	v_fmac_f32_e32 v16, v18, v18
	v_cvt_pk_bf16_f32 v10, v20, v21
	v_cvt_pk_bf16_f32 v11, v18, v19
	v_add_f32_e32 v15, v15, v16
	v_and_b32_e32 v16, 0xffff0000, v246
	v_and_b32_e32 v18, 0xffff0000, v247
	v_add_f32_e32 v14, v14, v15
	v_lshlrev_b32_e32 v15, 16, v246
	v_lshlrev_b32_e32 v17, 16, v247
	v_lshlrev_b32_e32 v19, 16, v248
	v_and_b32_e32 v20, 0xffff0000, v248
	v_add_f32_e32 v5, v5, v16
	v_add_f32_e32 v18, v7, v18
	v_and_b32_e32 v22, 0xffff0000, v249
	v_add_f32_e32 v4, v4, v15
	v_add_f32_e32 v15, v0, v19
	v_add_f32_e32 v16, v1, v20
	v_add_f32_e32 v17, v6, v17
	v_mul_f32_e32 v0, v5, v5
	v_mul_f32_e32 v1, v18, v18
	v_lshlrev_b32_e32 v21, 16, v249
	v_add_f32_e32 v20, v3, v22
	v_fmac_f32_e32 v0, v4, v4
	v_fmac_f32_e32 v1, v17, v17
	v_add_f32_e32 v19, v2, v21
	v_add_f32_e32 v0, v0, v1
	v_mul_f32_e32 v1, v16, v16
	v_mul_f32_e32 v2, v20, v20
	v_fmac_f32_e32 v1, v15, v15
	v_fmac_f32_e32 v2, v19, v19
	v_add_f32_e32 v1, v1, v2
	v_add_f32_e32 v0, v0, v1
	v_add_f32_e32 v3, v14, v0
	ds_bpermute_b32 v14, v112, v3
	v_lshl_add_u64 v[12:13], s[10:11], 0, v[90:91]
	v_lshl_add_u64 v[12:13], s[28:29], 1, v[12:13]
	v_lshl_add_u64 v[0:1], v[12:13], 0, s[6:7]
	v_lshl_add_u64 v[6:7], v[0:1], 0, v[160:161]
	s_waitcnt lgkmcnt(0)
	v_add_f32_e32 v0, v3, v14
	ds_bpermute_b32 v1, v113, v0
	global_store_dwordx4 v[6:7], v[8:11], off
	v_cvt_pk_bf16_f32 v2, v4, v5
	v_cvt_pk_bf16_f32 v3, v17, v18
	v_cvt_pk_bf16_f32 v4, v15, v16
	v_cvt_pk_bf16_f32 v5, v19, v20
	global_store_dwordx4 v[6:7], v[2:5], off offset:256
	s_and_saveexec_b64 s[28:29], s[2:3]
	s_cbranch_execz .LBB0_1799
	v_lshlrev_b64 v[2:3], 6, v[88:89]
	v_lshl_add_u64 v[2:3], s[12:13], 0, v[2:3]
	v_lshl_add_u64 v[2:3], s[26:27], 2, v[2:3]
	s_lshl_b32 s26, s46, 2
	s_mov_b32 s27, s7
	v_lshl_add_u64 v[2:3], v[2:3], 0, s[26:27]
	s_waitcnt lgkmcnt(0)
	v_add_f32_e32 v0, v0, v1
	global_store_dword v[2:3], v0, off

;     __device__ __forceinline__ void operator()(const f32x4 (&acc)[2][2][4][2], const Unit& u, int wr, int wc, int fr, int fq) const {
;     ...
;             if (RES_BF16) {
; #pragma unroll
;                 for (int m = 0; m < 4; ++m)
; #pragma unroll
;                     for (int bj = 0; bj < 2; ++bj)
;                         rw[m][bj] = *(const u32x4*)(xb + (size_t)(u.pm * BM + ai * HALF + wr * 64 + m * 16 + fr) * 1024 + u.pn * BM + bj * HALF + wc * 32 + 8 * fq);
; #pragma unroll
;                 for (int m = 0; m < 4; ++m)
; #pragma unroll
;                     for (int bj = 0; bj < 2; ++bj) asm volatile("" : "+v"(rw[m][bj]));
;             }
; #pragma unroll
;             for (int m = 0; m < 4; ++m) {
;                 const int row = u.pm * BM + ai * HALF + wr * 64 + m * 16 + fr;
;                 float s = 0.f;
; #pragma unroll
;                 for (int bj = 0; bj < 2; ++bj) {
;                     const size_t off = (size_t)row * 1024 + u.pn * BM + bj * HALF + wc * 32 + 8 * fq;
;                     f32x4 r0, r1;
;                     if (RES_BF16) {
;                         const u32x4 w_ = rw[m][bj];
;                         r0 = (f32x4){__uint_as_float(w_.x << 16), __uint_as_float(w_.x & 0xffff0000u), __uint_as_float(w_.y << 16), __uint_as_float(w_.y & 0xffff0000u)};
;                         r1 = (f32x4){__uint_as_float(w_.z << 16), __uint_as_float(w_.z & 0xffff0000u), __uint_as_float(w_.w << 16), __uint_as_float(w_.w & 0xffff0000u)};
;                     } else { r0 = *(const f32x4*)(resid + off); r1 = *(const f32x4*)(resid + off + 4); }
;                     f32x4 v0, v1;
; #pragma unroll
;                     for (int j = 0; j < 4; ++j) { v0[j] = acc[ai][bj][m][0][j] + r0[j]; v1[j] = acc[ai][bj][m][1][j] + r1[j]; }
;                     if (OUT_F32) { *(f32x4*)(xout + off) = v0; *(f32x4*)(xout + off + 4) = v1; }
;                     else {
;                         u32x4 w; w.x = cvt_pk_bf16(v0[0], v0[1]); w.y = cvt_pk_bf16(v0[2], v0[3]); w.z = cvt_pk_bf16(v1[0], v1[1]); w.w = cvt_pk_bf16(v1[2], v1[3]);
;                         *(u32x4*)(xb + off) = w;
;                     }
;                     s += dot4(v0) + dot4(v1);
;                 }
;                 s += __shfl_xor(s, 16); s += __shfl_xor(s, 32);
;                 if (fq == 0) ssq[(size_t)row * 16 + u.pn * 4 + wc] = s;
.LBB0_1955:
	s_lshl_b32 s24, s64, 8
	v_lshl_add_u32 v172, s65, 8, v188
	s_ashr_i32 s25, s24, 31
	s_lshl_b64 s[26:27], s[24:25], 1
	v_ashrrev_i32_e32 v173, 31, v172
	v_lshl_add_u64 v[174:175], v[162:163], 0, s[26:27]
	v_lshlrev_b64 v[202:203], 11, v[172:173]
	v_lshl_add_u64 v[128:129], v[174:175], 0, v[202:203]
	v_or_b32_e32 v184, 16, v172
	global_load_dwordx4 v[194:197], v[128:129], off
	global_load_dwordx4 v[198:201], v[128:129], off offset:256
	v_ashrrev_i32_e32 v185, 31, v184
	v_or_b32_e32 v180, 32, v172
	v_lshlrev_b64 v[186:187], 11, v[184:185]
	v_ashrrev_i32_e32 v181, 31, v180
	v_or_b32_e32 v176, 48, v172
	v_lshl_add_u64 v[128:129], v[174:175], 0, v[186:187]
	v_lshlrev_b64 v[182:183], 11, v[180:181]
	v_ashrrev_i32_e32 v177, 31, v176
	global_load_dwordx4 v[148:151], v[128:129], off
	global_load_dwordx4 v[144:147], v[128:129], off offset:256
	v_lshl_add_u64 v[128:129], v[174:175], 0, v[182:183]
	v_lshlrev_b64 v[178:179], 11, v[176:177]
	global_load_dwordx4 v[140:143], v[128:129], off
	global_load_dwordx4 v[136:139], v[128:129], off offset:256
	v_lshl_add_u64 v[128:129], v[174:175], 0, v[178:179]
	global_load_dwordx4 v[132:135], v[128:129], off
	s_nop 0
	global_load_dwordx4 v[128:131], v[128:129], off offset:256
	v_add_u32_e32 v250, 0x80, v172
	v_ashrrev_i32_e32 v251, 31, v250
	v_lshlrev_b64 v[250:251], 11, v[250:251]
	v_lshl_add_u64 v[250:251], v[174:175], 0, v[250:251]
	global_load_dwordx4 v[218:221], v[250:251], off
	global_load_dwordx4 v[222:225], v[250:251], off offset:256
	v_add_u32_e32 v250, 0x90, v172
	v_ashrrev_i32_e32 v251, 31, v250
	v_lshlrev_b64 v[250:251], 11, v[250:251]
	v_lshl_add_u64 v[250:251], v[174:175], 0, v[250:251]
	global_load_dwordx4 v[226:229], v[250:251], off
	global_load_dwordx4 v[230:233], v[250:251], off offset:256
	v_add_u32_e32 v250, 0xa0, v172
	v_ashrrev_i32_e32 v251, 31, v250
	v_lshlrev_b64 v[250:251], 11, v[250:251]
	v_lshl_add_u64 v[250:251], v[174:175], 0, v[250:251]
	global_load_dwordx4 v[234:237], v[250:251], off
	global_load_dwordx4 v[238:241], v[250:251], off offset:256
	v_add_u32_e32 v250, 0xb0, v172
	v_ashrrev_i32_e32 v251, 31, v250
	v_lshlrev_b64 v[250:251], 11, v[250:251]
	v_lshl_add_u64 v[250:251], v[174:175], 0, v[250:251]
	global_load_dwordx4 v[242:245], v[250:251], off
	global_load_dwordx4 v[246:249], v[250:251], off offset:256
	v_lshl_add_u64 v[202:203], s[12:13], 0, v[202:203]
	v_lshl_add_u64 v[202:203], v[202:203], 0, s[26:27]
	s_lshl_b32 s22, s64, 2
	s_ashr_i32 s23, s22, 31
	s_waitcnt vmcnt(8)
	s_nop 0
	v_lshlrev_b32_e32 v204, 16, v194
	v_and_b32_e32 v194, 0xffff0000, v194
	v_lshlrev_b32_e32 v205, 16, v195
	v_and_b32_e32 v195, 0xffff0000, v195
	v_lshlrev_b32_e32 v206, 16, v196
	v_and_b32_e32 v196, 0xffff0000, v196
	v_lshlrev_b32_e32 v207, 16, v197
	v_and_b32_e32 v197, 0xffff0000, v197
	v_lshlrev_b32_e32 v208, 16, v198
	v_and_b32_e32 v198, 0xffff0000, v198
	v_lshlrev_b32_e32 v209, 16, v199
	v_and_b32_e32 v199, 0xffff0000, v199
	v_lshlrev_b32_e32 v210, 16, v200
	v_and_b32_e32 v200, 0xffff0000, v200
	v_add_f32_e32 v125, v125, v194
	v_add_f32_e32 v121, v121, v196
	v_add_f32_e32 v127, v127, v195
	v_add_f32_e32 v123, v123, v197
	v_add_f32_e32 v124, v124, v204
	v_add_f32_e32 v120, v120, v206
	v_add_f32_e32 v126, v126, v205
	v_add_f32_e32 v122, v122, v207
	v_add_f32_e32 v195, v112, v210
	v_add_f32_e32 v196, v117, v198
	v_add_f32_e32 v197, v113, v200
	v_add_f32_e32 v198, v118, v209
	v_add_f32_e32 v199, v119, v199
	v_mul_f32_e32 v112, v125, v125
	v_mul_f32_e32 v113, v127, v127
	v_mul_f32_e32 v118, v121, v121
	v_mul_f32_e32 v119, v123, v123
	v_lshlrev_b32_e32 v211, 16, v201
	v_and_b32_e32 v201, 0xffff0000, v201
	v_fmac_f32_e32 v112, v124, v124
	v_fmac_f32_e32 v113, v126, v126
	v_fmac_f32_e32 v118, v120, v120
	v_fmac_f32_e32 v119, v122, v122
	v_add_f32_e32 v201, v115, v201
	v_add_f32_e32 v112, v112, v113
	v_add_f32_e32 v113, v118, v119
	v_add_f32_e32 v194, v116, v208
	v_add_f32_e32 v200, v114, v211
	v_cvt_pk_bf16_f32 v114, v124, v125
	v_cvt_pk_bf16_f32 v115, v126, v127
	v_cvt_pk_bf16_f32 v116, v120, v121
	v_cvt_pk_bf16_f32 v117, v122, v123
	v_mul_f32_e32 v121, v196, v196
	v_mul_f32_e32 v123, v199, v199
	v_add_f32_e32 v112, v112, v113
	v_mul_f32_e32 v113, v197, v197
	v_mul_f32_e32 v119, v201, v201
	v_fmac_f32_e32 v121, v194, v194
	v_fmac_f32_e32 v123, v198, v198
	v_fmac_f32_e32 v113, v195, v195
	v_fmac_f32_e32 v119, v200, v200
	v_add_f32_e32 v118, v121, v123
	v_add_f32_e32 v113, v113, v119
	v_add_f32_e32 v113, v118, v113
	v_and_b32_e32 v118, 64, v193
	v_add_f32_e32 v113, v112, v113
	v_xor_b32_e32 v112, 16, v193
	v_add_u32_e32 v122, 64, v118
	v_cmp_lt_i32_e32 vcc, v112, v122
	v_lshl_add_u64 v[118:119], v[202:203], 0, s[8:9]
	v_lshl_add_u64 v[120:121], v[118:119], 0, v[160:161]
	v_cndmask_b32_e32 v112, v193, v112, vcc
	v_lshlrev_b32_e32 v112, 2, v112
	ds_bpermute_b32 v123, v112, v113
	global_store_dwordx4 v[120:121], v[114:117], off
	s_nop 1
	v_cvt_pk_bf16_f32 v116, v194, v196
	s_waitcnt lgkmcnt(0)
	v_add_f32_e32 v114, v113, v123
	v_xor_b32_e32 v113, 32, v193
	v_cmp_lt_i32_e32 vcc, v113, v122
	v_cvt_pk_bf16_f32 v117, v198, v199
	v_cvt_pk_bf16_f32 v118, v195, v197
	v_cvt_pk_bf16_f32 v119, v200, v201
	global_store_dwordx4 v[120:121], v[116:119], off offset:256
	s_nop 0
	v_cndmask_b32_e32 v113, v193, v113, vcc
	v_lshlrev_b32_e32 v113, 2, v113
	ds_bpermute_b32 v115, v113, v114
	s_and_saveexec_b64 s[26:27], s[2:3]
	s_cbranch_execz .LBB0_1957
	v_lshlrev_b64 v[116:117], 6, v[172:173]
	v_lshl_add_u64 v[116:117], s[14:15], 0, v[116:117]
	v_lshl_add_u64 v[116:117], s[22:23], 2, v[116:117]
	s_lshl_b32 s28, s38, 2
	s_mov_b32 s29, s9
	v_lshl_add_u64 v[116:117], v[116:117], 0, s[28:29]
	s_waitcnt lgkmcnt(0)
	v_add_f32_e32 v114, v114, v115
	global_store_dword v[116:117], v114, off

; __device__ __forceinline__ unsigned cvt_pk_bf16(float lo, float hi) { unsigned r; asm volatile("v_cvt_pk_bf16_f32 %0, %1, %2" : "=v"(r) : "v"(lo), "v"(hi)); return r; }
; __device__ __forceinline__ float dot4(f32x4 v) { return (v.x * v.x + v.y * v.y) + (v.z * v.z + v.w * v.w); }
;     __device__ __forceinline__ void operator()(const f32x4 (&acc)[2][2][4][2], const Unit& u, int wr, int wc, int fr, int fq) const {
;     ...
;             for (int m = 0; m < 4; ++m) {
;                 const int row = u.pm * BM + ai * HALF + wr * 64 + m * 16 + fr;
;                 float s = 0.f;
; #pragma unroll
;                 for (int bj = 0; bj < 2; ++bj) {
;                     const size_t off = (size_t)row * 1024 + u.pn * BM + bj * HALF + wc * 32 + 8 * fq;
;                     f32x4 r0, r1;
;                     if (RES_BF16) {
;                         const u32x4 w_ = rw[m][bj];
;                         r0 = (f32x4){__uint_as_float(w_.x << 16), __uint_as_float(w_.x & 0xffff0000u), __uint_as_float(w_.y << 16), __uint_as_float(w_.y & 0xffff0000u)};
;                         r1 = (f32x4){__uint_as_float(w_.z << 16), __uint_as_float(w_.z & 0xffff0000u), __uint_as_float(w_.w << 16), __uint_as_float(w_.w & 0xffff0000u)};
;                     } else { r0 = *(const f32x4*)(resid + off); r1 = *(const f32x4*)(resid + off + 4); }
;                     f32x4 v0, v1;
; #pragma unroll
;                     for (int j = 0; j < 4; ++j) { v0[j] = acc[ai][bj][m][0][j] + r0[j]; v1[j] = acc[ai][bj][m][1][j] + r1[j]; }
;                     if (OUT_F32) { *(f32x4*)(xout + off) = v0; *(f32x4*)(xout + off + 4) = v1; }
;                     else {
;                         u32x4 w; w.x = cvt_pk_bf16(v0[0], v0[1]); w.y = cvt_pk_bf16(v0[2], v0[3]); w.z = cvt_pk_bf16(v1[0], v1[1]); w.w = cvt_pk_bf16(v1[2], v1[3]);
;                         *(u32x4*)(xb + off) = w;
;                     }
;                     s += dot4(v0) + dot4(v1);
;                 }
;                 s += __shfl_xor(s, 16); s += __shfl_xor(s, 32);
;                 if (fq == 0) ssq[(size_t)row * 16 + u.pn * 4 + wc] = s;
.LBB0_1963:
	s_or_b64 exec, exec, s[26:27]
	v_add_u32_e32 v100, 0x80, v172
	v_ashrrev_i32_e32 v101, 31, v100
	v_add_u32_e32 v96, 0x90, v172
	v_lshlrev_b64 v[110:111], 11, v[100:101]
	v_ashrrev_i32_e32 v97, 31, v96
	v_add_u32_e32 v92, 0xa0, v172
	s_waitcnt lgkmcnt(0)
	v_lshlrev_b64 v[98:99], 11, v[96:97]
	v_ashrrev_i32_e32 v93, 31, v92
	v_add_u32_e32 v88, 0xb0, v172
	v_lshlrev_b64 v[94:95], 11, v[92:93]
	v_ashrrev_i32_e32 v89, 31, v88
	v_lshlrev_b64 v[90:91], 11, v[88:89]
	v_lshl_add_u64 v[110:111], s[12:13], 0, v[110:111]
	v_lshl_add_u64 v[110:111], s[24:25], 1, v[110:111]
	s_waitcnt vmcnt(8)
	v_lshlrev_b32_e32 v114, 16, v218
	v_and_b32_e32 v102, 0xffff0000, v218
	v_lshlrev_b32_e32 v115, 16, v219
	v_and_b32_e32 v103, 0xffff0000, v219
	v_lshlrev_b32_e32 v116, 16, v220
	v_and_b32_e32 v104, 0xffff0000, v220
	v_lshlrev_b32_e32 v117, 16, v221
	v_and_b32_e32 v105, 0xffff0000, v221
	v_lshlrev_b32_e32 v118, 16, v222
	v_and_b32_e32 v106, 0xffff0000, v222
	v_lshlrev_b32_e32 v119, 16, v223
	v_and_b32_e32 v107, 0xffff0000, v223
	v_lshlrev_b32_e32 v120, 16, v224
	v_and_b32_e32 v108, 0xffff0000, v224
	v_lshlrev_b32_e32 v121, 16, v225
	v_and_b32_e32 v109, 0xffff0000, v225
	v_add_f32_e32 v61, v61, v102
	v_add_f32_e32 v57, v57, v104
	v_add_f32_e32 v63, v63, v103
	v_add_f32_e32 v59, v59, v105
	v_add_f32_e32 v104, v53, v106
	v_add_f32_e32 v105, v49, v108
	v_add_f32_e32 v107, v55, v107
	v_add_f32_e32 v109, v51, v109
	v_add_f32_e32 v60, v60, v114
	v_add_f32_e32 v56, v56, v116
	v_add_f32_e32 v62, v62, v115
	v_add_f32_e32 v58, v58, v117
	v_add_f32_e32 v102, v52, v118
	v_add_f32_e32 v103, v48, v120
	v_add_f32_e32 v106, v54, v119
	v_add_f32_e32 v108, v50, v121
	v_cvt_pk_bf16_f32 v48, v60, v61
	v_cvt_pk_bf16_f32 v49, v62, v63
	v_cvt_pk_bf16_f32 v50, v56, v57
	v_cvt_pk_bf16_f32 v51, v58, v59
	v_mul_f32_e32 v52, v61, v61
	v_mul_f32_e32 v53, v63, v63
	v_mul_f32_e32 v54, v57, v57
	v_mul_f32_e32 v55, v59, v59
	v_mul_f32_e32 v57, v104, v104
	v_mul_f32_e32 v59, v107, v107
	v_mul_f32_e32 v61, v105, v105
	v_mul_f32_e32 v63, v109, v109
	v_fmac_f32_e32 v52, v60, v60
	v_fmac_f32_e32 v53, v62, v62
	v_fmac_f32_e32 v54, v56, v56
	v_fmac_f32_e32 v55, v58, v58
	v_fmac_f32_e32 v57, v102, v102
	v_fmac_f32_e32 v59, v106, v106
	v_fmac_f32_e32 v61, v103, v103
	v_fmac_f32_e32 v63, v108, v108
	v_add_f32_e32 v52, v52, v53
	v_add_f32_e32 v53, v54, v55
	v_add_f32_e32 v54, v57, v59
	v_add_f32_e32 v55, v61, v63
	v_add_f32_e32 v52, v52, v53
	v_add_f32_e32 v53, v54, v55
	v_add_f32_e32 v56, v52, v53
	ds_bpermute_b32 v57, v112, v56
	v_lshl_add_u64 v[52:53], v[110:111], 0, s[8:9]
	v_lshl_add_u64 v[54:55], v[52:53], 0, v[160:161]
	global_store_dwordx4 v[54:55], v[48:51], off
	s_waitcnt lgkmcnt(0)
	s_nop 0
	v_add_f32_e32 v48, v56, v57
	ds_bpermute_b32 v49, v113, v48
	v_cvt_pk_bf16_f32 v50, v102, v104
	v_cvt_pk_bf16_f32 v51, v106, v107
	v_cvt_pk_bf16_f32 v52, v103, v105
	v_cvt_pk_bf16_f32 v53, v108, v109
	global_store_dwordx4 v[54:55], v[50:53], off offset:256
	s_and_saveexec_b64 s[26:27], s[2:3]
	s_cbranch_execz .LBB0_1965
	v_lshlrev_b64 v[50:51], 6, v[100:101]
	v_lshl_add_u64 v[50:51], s[14:15], 0, v[50:51]
	v_lshl_add_u64 v[50:51], s[22:23], 2, v[50:51]
	s_lshl_b32 s28, s38, 2
	s_mov_b32 s29, s9
	v_lshl_add_u64 v[50:51], v[50:51], 0, s[28:29]
	s_waitcnt lgkmcnt(0)
	v_add_f32_e32 v48, v48, v49
	global_store_dword v[50:51], v48, off
.LBB0_1965:
	s_or_b64 exec, exec, s[26:27]
	s_waitcnt lgkmcnt(0)
	v_and_b32_e32 v49, 0xffff0000, v226
	v_and_b32_e32 v51, 0xffff0000, v227
	v_lshlrev_b32_e32 v48, 16, v226
	v_lshlrev_b32_e32 v50, 16, v227
	v_lshlrev_b32_e32 v52, 16, v228
	v_and_b32_e32 v53, 0xffff0000, v228
	v_add_f32_e32 v49, v45, v49
	v_add_f32_e32 v47, v47, v51
	v_and_b32_e32 v55, 0xffff0000, v229
	v_add_f32_e32 v48, v44, v48
	v_add_f32_e32 v52, v40, v52
	v_add_f32_e32 v53, v41, v53
	v_add_f32_e32 v46, v46, v50
	v_cvt_pk_bf16_f32 v40, v48, v49
	v_cvt_pk_bf16_f32 v41, v46, v47
	v_mul_f32_e32 v49, v49, v49
	v_mul_f32_e32 v47, v47, v47
	v_lshlrev_b32_e32 v54, 16, v229
	v_add_f32_e32 v51, v43, v55
	v_fmac_f32_e32 v49, v48, v48
	v_fmac_f32_e32 v47, v46, v46
	v_add_f32_e32 v50, v42, v54
	v_add_f32_e32 v46, v49, v47
	v_mul_f32_e32 v47, v53, v53
	v_mul_f32_e32 v48, v51, v51
	v_fmac_f32_e32 v47, v52, v52
	v_fmac_f32_e32 v48, v50, v50
	v_cvt_pk_bf16_f32 v42, v52, v53
	v_cvt_pk_bf16_f32 v43, v50, v51
	v_add_f32_e32 v47, v47, v48
	v_and_b32_e32 v48, 0xffff0000, v230
	v_and_b32_e32 v50, 0xffff0000, v231
	v_add_f32_e32 v46, v46, v47
	v_lshlrev_b32_e32 v47, 16, v230
	v_lshlrev_b32_e32 v49, 16, v231
	v_lshlrev_b32_e32 v51, 16, v232
	v_and_b32_e32 v52, 0xffff0000, v232
	v_add_f32_e32 v37, v37, v48
	v_add_f32_e32 v50, v39, v50
	v_and_b32_e32 v54, 0xffff0000, v233
	v_add_f32_e32 v36, v36, v47
	v_add_f32_e32 v47, v32, v51
	v_add_f32_e32 v48, v33, v52
	v_add_f32_e32 v49, v38, v49
	v_mul_f32_e32 v32, v37, v37
	v_mul_f32_e32 v33, v50, v50
	v_lshlrev_b32_e32 v53, 16, v233
	v_add_f32_e32 v52, v35, v54
	v_fmac_f32_e32 v32, v36, v36
	v_fmac_f32_e32 v33, v49, v49
	v_add_f32_e32 v51, v34, v53
	v_add_f32_e32 v32, v32, v33
	v_mul_f32_e32 v33, v48, v48
	v_mul_f32_e32 v34, v52, v52
	v_fmac_f32_e32 v33, v47, v47
	v_fmac_f32_e32 v34, v51, v51
	v_add_f32_e32 v33, v33, v34
	v_add_f32_e32 v32, v32, v33
	v_add_f32_e32 v35, v46, v32
	ds_bpermute_b32 v46, v112, v35
	v_lshl_add_u64 v[44:45], s[12:13], 0, v[98:99]
	v_lshl_add_u64 v[44:45], s[24:25], 1, v[44:45]
	v_lshl_add_u64 v[32:33], v[44:45], 0, s[8:9]
	v_lshl_add_u64 v[38:39], v[32:33], 0, v[160:161]
	s_waitcnt lgkmcnt(0)
	v_add_f32_e32 v32, v35, v46
	ds_bpermute_b32 v33, v113, v32
	global_store_dwordx4 v[38:39], v[40:43], off
	v_cvt_pk_bf16_f32 v34, v36, v37
	v_cvt_pk_bf16_f32 v35, v49, v50
	v_cvt_pk_bf16_f32 v36, v47, v48
	v_cvt_pk_bf16_f32 v37, v51, v52
	global_store_dwordx4 v[38:39], v[34:37], off offset:256
	s_and_saveexec_b64 s[26:27], s[2:3]
	s_cbranch_execz .LBB0_1967
	v_lshlrev_b64 v[34:35], 6, v[96:97]
	v_lshl_add_u64 v[34:35], s[14:15], 0, v[34:35]
	v_lshl_add_u64 v[34:35], s[22:23], 2, v[34:35]
	s_lshl_b32 s28, s38, 2
	s_mov_b32 s29, s9
	v_lshl_add_u64 v[34:35], v[34:35], 0, s[28:29]
	s_waitcnt lgkmcnt(0)
	v_add_f32_e32 v32, v32, v33
	global_store_dword v[34:35], v32, off
; __device__ __forceinline__ unsigned cvt_pk_bf16(float lo, float hi) { unsigned r; asm volatile("v_cvt_pk_bf16_f32 %0, %1, %2" : "=v"(r) : "v"(lo), "v"(hi)); return r; }
; __device__ __forceinline__ float dot4(f32x4 v) { return (v.x * v.x + v.y * v.y) + (v.z * v.z + v.w * v.w); }
;     __device__ __forceinline__ void operator()(const f32x4 (&acc)[2][2][4][2], const Unit& u, int wr, int wc, int fr, int fq) const {
;     ...
;             for (int m = 0; m < 4; ++m) {
;                 const int row = u.pm * BM + ai * HALF + wr * 64 + m * 16 + fr;
;                 float s = 0.f;
; #pragma unroll
;                 for (int bj = 0; bj < 2; ++bj) {
;                     const size_t off = (size_t)row * 1024 + u.pn * BM + bj * HALF + wc * 32 + 8 * fq;
;                     f32x4 r0, r1;
;                     if (RES_BF16) {
;                         const u32x4 w_ = rw[m][bj];
;                         r0 = (f32x4){__uint_as_float(w_.x << 16), __uint_as_float(w_.x & 0xffff0000u), __uint_as_float(w_.y << 16), __uint_as_float(w_.y & 0xffff0000u)};
;                         r1 = (f32x4){__uint_as_float(w_.z << 16), __uint_as_float(w_.z & 0xffff0000u), __uint_as_float(w_.w << 16), __uint_as_float(w_.w & 0xffff0000u)};
;                     } else { r0 = *(const f32x4*)(resid + off); r1 = *(const f32x4*)(resid + off + 4); }
;                     f32x4 v0, v1;
; #pragma unroll
;                     for (int j = 0; j < 4; ++j) { v0[j] = acc[ai][bj][m][0][j] + r0[j]; v1[j] = acc[ai][bj][m][1][j] + r1[j]; }
;                     if (OUT_F32) { *(f32x4*)(xout + off) = v0; *(f32x4*)(xout + off + 4) = v1; }
;                     else {
;                         u32x4 w; w.x = cvt_pk_bf16(v0[0], v0[1]); w.y = cvt_pk_bf16(v0[2], v0[3]); w.z = cvt_pk_bf16(v1[0], v1[1]); w.w = cvt_pk_bf16(v1[2], v1[3]);
;                         *(u32x4*)(xb + off) = w;
;                     }
;                     s += dot4(v0) + dot4(v1);
;                 }
;                 s += __shfl_xor(s, 16); s += __shfl_xor(s, 32);
;                 if (fq == 0) ssq[(size_t)row * 16 + u.pn * 4 + wc] = s;
.LBB0_1967:
	s_or_b64 exec, exec, s[26:27]
	s_waitcnt lgkmcnt(0)
	v_and_b32_e32 v33, 0xffff0000, v234
	v_and_b32_e32 v35, 0xffff0000, v235
	v_lshlrev_b32_e32 v32, 16, v234
	v_lshlrev_b32_e32 v34, 16, v235
	v_lshlrev_b32_e32 v36, 16, v236
	v_and_b32_e32 v37, 0xffff0000, v236
	v_add_f32_e32 v33, v29, v33
	v_add_f32_e32 v31, v31, v35
	v_and_b32_e32 v39, 0xffff0000, v237
	v_add_f32_e32 v32, v28, v32
	v_add_f32_e32 v36, v24, v36
	v_add_f32_e32 v37, v25, v37
	v_add_f32_e32 v30, v30, v34
	v_cvt_pk_bf16_f32 v24, v32, v33
	v_cvt_pk_bf16_f32 v25, v30, v31
	v_mul_f32_e32 v33, v33, v33
	v_mul_f32_e32 v31, v31, v31
	v_lshlrev_b32_e32 v38, 16, v237
	v_add_f32_e32 v35, v27, v39
	v_fmac_f32_e32 v33, v32, v32
	v_fmac_f32_e32 v31, v30, v30
	v_add_f32_e32 v34, v26, v38
	v_add_f32_e32 v30, v33, v31
	v_mul_f32_e32 v31, v37, v37
	v_mul_f32_e32 v32, v35, v35
	v_fmac_f32_e32 v31, v36, v36
	v_fmac_f32_e32 v32, v34, v34
	v_cvt_pk_bf16_f32 v26, v36, v37
	v_cvt_pk_bf16_f32 v27, v34, v35
	v_add_f32_e32 v31, v31, v32
	v_and_b32_e32 v32, 0xffff0000, v238
	v_and_b32_e32 v34, 0xffff0000, v239
	v_add_f32_e32 v30, v30, v31
	v_lshlrev_b32_e32 v31, 16, v238
	v_lshlrev_b32_e32 v33, 16, v239
	v_lshlrev_b32_e32 v35, 16, v240
	v_and_b32_e32 v36, 0xffff0000, v240
	v_add_f32_e32 v21, v21, v32
	v_add_f32_e32 v34, v23, v34
	v_and_b32_e32 v38, 0xffff0000, v241
	v_add_f32_e32 v20, v20, v31
	v_add_f32_e32 v31, v16, v35
	v_add_f32_e32 v32, v17, v36
	v_add_f32_e32 v33, v22, v33
	v_mul_f32_e32 v16, v21, v21
	v_mul_f32_e32 v17, v34, v34
	v_lshlrev_b32_e32 v37, 16, v241
	v_add_f32_e32 v36, v19, v38
	v_fmac_f32_e32 v16, v20, v20
	v_fmac_f32_e32 v17, v33, v33
	v_add_f32_e32 v35, v18, v37
	v_add_f32_e32 v16, v16, v17
	v_mul_f32_e32 v17, v32, v32
	v_mul_f32_e32 v18, v36, v36
	v_fmac_f32_e32 v17, v31, v31
	v_fmac_f32_e32 v18, v35, v35
	v_add_f32_e32 v17, v17, v18
	v_add_f32_e32 v16, v16, v17
	v_add_f32_e32 v19, v30, v16
	ds_bpermute_b32 v30, v112, v19
	v_lshl_add_u64 v[28:29], s[12:13], 0, v[94:95]
	v_lshl_add_u64 v[28:29], s[24:25], 1, v[28:29]
	v_lshl_add_u64 v[16:17], v[28:29], 0, s[8:9]
	v_lshl_add_u64 v[22:23], v[16:17], 0, v[160:161]
	s_waitcnt lgkmcnt(0)
	v_add_f32_e32 v16, v19, v30
	ds_bpermute_b32 v17, v113, v16
	global_store_dwordx4 v[22:23], v[24:27], off
	v_cvt_pk_bf16_f32 v18, v20, v21
	v_cvt_pk_bf16_f32 v19, v33, v34
	v_cvt_pk_bf16_f32 v20, v31, v32
	v_cvt_pk_bf16_f32 v21, v35, v36
	global_store_dwordx4 v[22:23], v[18:21], off offset:256
	s_and_saveexec_b64 s[26:27], s[2:3]
	s_cbranch_execz .LBB0_1969
	v_lshlrev_b64 v[18:19], 6, v[92:93]
	v_lshl_add_u64 v[18:19], s[14:15], 0, v[18:19]
	v_lshl_add_u64 v[18:19], s[22:23], 2, v[18:19]
	s_lshl_b32 s28, s38, 2
	s_mov_b32 s29, s9
	v_lshl_add_u64 v[18:19], v[18:19], 0, s[28:29]
	s_waitcnt lgkmcnt(0)
	v_add_f32_e32 v16, v16, v17
	global_store_dword v[18:19], v16, off
.LBB0_1969:
	s_or_b64 exec, exec, s[26:27]
	s_waitcnt lgkmcnt(0)
	v_and_b32_e32 v17, 0xffff0000, v242
	v_and_b32_e32 v19, 0xffff0000, v243
	v_lshlrev_b32_e32 v16, 16, v242
	v_lshlrev_b32_e32 v18, 16, v243
	v_lshlrev_b32_e32 v20, 16, v244
	v_and_b32_e32 v21, 0xffff0000, v244
	v_add_f32_e32 v17, v13, v17
	v_add_f32_e32 v15, v15, v19
	v_and_b32_e32 v23, 0xffff0000, v245
	v_add_f32_e32 v16, v12, v16
	v_add_f32_e32 v20, v8, v20
	v_add_f32_e32 v21, v9, v21
	v_add_f32_e32 v14, v14, v18
	v_cvt_pk_bf16_f32 v8, v16, v17
	v_cvt_pk_bf16_f32 v9, v14, v15
	v_mul_f32_e32 v17, v17, v17
	v_mul_f32_e32 v15, v15, v15
	v_lshlrev_b32_e32 v22, 16, v245
	v_add_f32_e32 v19, v11, v23
	v_fmac_f32_e32 v17, v16, v16
	v_fmac_f32_e32 v15, v14, v14
	v_add_f32_e32 v18, v10, v22
	v_add_f32_e32 v14, v17, v15
	v_mul_f32_e32 v15, v21, v21
	v_mul_f32_e32 v16, v19, v19
	v_fmac_f32_e32 v15, v20, v20
	v_fmac_f32_e32 v16, v18, v18
	v_cvt_pk_bf16_f32 v10, v20, v21
	v_cvt_pk_bf16_f32 v11, v18, v19
	v_add_f32_e32 v15, v15, v16
	v_and_b32_e32 v16, 0xffff0000, v246
	v_and_b32_e32 v18, 0xffff0000, v247
	v_add_f32_e32 v14, v14, v15
	v_lshlrev_b32_e32 v15, 16, v246
	v_lshlrev_b32_e32 v17, 16, v247
	v_lshlrev_b32_e32 v19, 16, v248
	v_and_b32_e32 v20, 0xffff0000, v248
	v_add_f32_e32 v5, v5, v16
	v_add_f32_e32 v18, v7, v18
	v_and_b32_e32 v22, 0xffff0000, v249
	v_add_f32_e32 v4, v4, v15
	v_add_f32_e32 v15, v0, v19
	v_add_f32_e32 v16, v1, v20
	v_add_f32_e32 v17, v6, v17
	v_mul_f32_e32 v0, v5, v5
	v_mul_f32_e32 v1, v18, v18
	v_lshlrev_b32_e32 v21, 16, v249
	v_add_f32_e32 v20, v3, v22
	v_fmac_f32_e32 v0, v4, v4
	v_fmac_f32_e32 v1, v17, v17
	v_add_f32_e32 v19, v2, v21
	v_add_f32_e32 v0, v0, v1
	v_mul_f32_e32 v1, v16, v16
	v_mul_f32_e32 v2, v20, v20
	v_fmac_f32_e32 v1, v15, v15
	v_fmac_f32_e32 v2, v19, v19
	v_add_f32_e32 v1, v1, v2
	v_add_f32_e32 v0, v0, v1
	v_add_f32_e32 v3, v14, v0
	ds_bpermute_b32 v14, v112, v3
	v_lshl_add_u64 v[12:13], s[12:13], 0, v[90:91]
	v_lshl_add_u64 v[12:13], s[24:25], 1, v[12:13]
	v_lshl_add_u64 v[0:1], v[12:13], 0, s[8:9]
	v_lshl_add_u64 v[6:7], v[0:1], 0, v[160:161]
	s_waitcnt lgkmcnt(0)
	v_add_f32_e32 v0, v3, v14
	ds_bpermute_b32 v1, v113, v0
	global_store_dwordx4 v[6:7], v[8:11], off
	v_cvt_pk_bf16_f32 v2, v4, v5
	v_cvt_pk_bf16_f32 v3, v17, v18
	v_cvt_pk_bf16_f32 v4, v15, v16
	v_cvt_pk_bf16_f32 v5, v19, v20
	global_store_dwordx4 v[6:7], v[2:5], off offset:256
	s_and_saveexec_b64 s[24:25], s[2:3]
	s_cbranch_execz .LBB0_1971
	v_lshlrev_b64 v[2:3], 6, v[88:89]
	v_lshl_add_u64 v[2:3], s[14:15], 0, v[2:3]
	v_lshl_add_u64 v[2:3], s[22:23], 2, v[2:3]
	s_lshl_b32 s22, s38, 2
	s_mov_b32 s23, s9
	v_lshl_add_u64 v[2:3], v[2:3], 0, s[22:23]
	s_waitcnt lgkmcnt(0)
	v_add_f32_e32 v0, v0, v1
	global_store_dword v[2:3], v0, off

;     __device__ __forceinline__ void operator()(const f32x4 (&acc)[2][2][4][2], const Unit& u, int wr, int wc, int fr, int fq) const {
;     ...
;             if (RES_BF16) {
; #pragma unroll
;                 for (int m = 0; m < 4; ++m)
; #pragma unroll
;                     for (int bj = 0; bj < 2; ++bj)
;                         rw[m][bj] = *(const u32x4*)(xb + (size_t)(u.pm * BM + ai * HALF + wr * 64 + m * 16 + fr) * 1024 + u.pn * BM + bj * HALF + wc * 32 + 8 * fq);
; #pragma unroll
;                 for (int m = 0; m < 4; ++m)
; #pragma unroll
;                     for (int bj = 0; bj < 2; ++bj) asm volatile("" : "+v"(rw[m][bj]));
;             }
; #pragma unroll
;             for (int m = 0; m < 4; ++m) {
;                 const int row = u.pm * BM + ai * HALF + wr * 64 + m * 16 + fr;
;                 float s = 0.f;
; #pragma unroll
;                 for (int bj = 0; bj < 2; ++bj) {
;                     const size_t off = (size_t)row * 1024 + u.pn * BM + bj * HALF + wc * 32 + 8 * fq;
;                     f32x4 r0, r1;
;                     if (RES_BF16) {
;                         const u32x4 w_ = rw[m][bj];
;                         r0 = (f32x4){__uint_as_float(w_.x << 16), __uint_as_float(w_.x & 0xffff0000u), __uint_as_float(w_.y << 16), __uint_as_float(w_.y & 0xffff0000u)};
;                         r1 = (f32x4){__uint_as_float(w_.z << 16), __uint_as_float(w_.z & 0xffff0000u), __uint_as_float(w_.w << 16), __uint_as_float(w_.w & 0xffff0000u)};
;                     } else { r0 = *(const f32x4*)(resid + off); r1 = *(const f32x4*)(resid + off + 4); }
;                     f32x4 v0, v1;
; #pragma unroll
;                     for (int j = 0; j < 4; ++j) { v0[j] = acc[ai][bj][m][0][j] + r0[j]; v1[j] = acc[ai][bj][m][1][j] + r1[j]; }
;                     if (OUT_F32) { *(f32x4*)(xout + off) = v0; *(f32x4*)(xout + off + 4) = v1; }
;                     else {
;                         u32x4 w; w.x = cvt_pk_bf16(v0[0], v0[1]); w.y = cvt_pk_bf16(v0[2], v0[3]); w.z = cvt_pk_bf16(v1[0], v1[1]); w.w = cvt_pk_bf16(v1[2], v1[3]);
;                         *(u32x4*)(xb + off) = w;
;                     }
;                     s += dot4(v0) + dot4(v1);
;                 }
;                 s += __shfl_xor(s, 16); s += __shfl_xor(s, 32);
;                 if (fq == 0) ssq[(size_t)row * 16 + u.pn * 4 + wc] = s;
.LBB0_2728:
	v_lshl_add_u32 v172, s28, 8, v188
	s_lshl_b32 s28, s26, 8
	s_ashr_i32 s29, s28, 31
	s_lshl_b64 s[30:31], s[28:29], 1
	v_ashrrev_i32_e32 v173, 31, v172
	v_lshl_add_u64 v[174:175], v[162:163], 0, s[30:31]
	v_lshlrev_b64 v[202:203], 11, v[172:173]
	v_lshl_add_u64 v[128:129], v[174:175], 0, v[202:203]
	v_or_b32_e32 v184, 16, v172
	global_load_dwordx4 v[194:197], v[128:129], off
	global_load_dwordx4 v[198:201], v[128:129], off offset:256
	v_ashrrev_i32_e32 v185, 31, v184
	v_or_b32_e32 v180, 32, v172
	v_lshlrev_b64 v[186:187], 11, v[184:185]
	v_ashrrev_i32_e32 v181, 31, v180
	v_or_b32_e32 v176, 48, v172
	v_lshl_add_u64 v[128:129], v[174:175], 0, v[186:187]
	v_lshlrev_b64 v[182:183], 11, v[180:181]
	v_ashrrev_i32_e32 v177, 31, v176
	global_load_dwordx4 v[148:151], v[128:129], off
	global_load_dwordx4 v[144:147], v[128:129], off offset:256
	v_lshl_add_u64 v[128:129], v[174:175], 0, v[182:183]
	v_lshlrev_b64 v[178:179], 11, v[176:177]
	global_load_dwordx4 v[140:143], v[128:129], off
	global_load_dwordx4 v[136:139], v[128:129], off offset:256
	v_lshl_add_u64 v[128:129], v[174:175], 0, v[178:179]
	global_load_dwordx4 v[132:135], v[128:129], off
	s_nop 0
	global_load_dwordx4 v[128:131], v[128:129], off offset:256
	v_add_u32_e32 v250, 0x80, v172
	v_ashrrev_i32_e32 v251, 31, v250
	v_lshlrev_b64 v[250:251], 11, v[250:251]
	v_lshl_add_u64 v[250:251], v[174:175], 0, v[250:251]
	global_load_dwordx4 v[218:221], v[250:251], off
	global_load_dwordx4 v[222:225], v[250:251], off offset:256
	v_add_u32_e32 v250, 0x90, v172
	v_ashrrev_i32_e32 v251, 31, v250
	v_lshlrev_b64 v[250:251], 11, v[250:251]
	v_lshl_add_u64 v[250:251], v[174:175], 0, v[250:251]
	global_load_dwordx4 v[226:229], v[250:251], off
	global_load_dwordx4 v[230:233], v[250:251], off offset:256
	v_add_u32_e32 v250, 0xa0, v172
	v_ashrrev_i32_e32 v251, 31, v250
	v_lshlrev_b64 v[250:251], 11, v[250:251]
	v_lshl_add_u64 v[250:251], v[174:175], 0, v[250:251]
	global_load_dwordx4 v[234:237], v[250:251], off
	global_load_dwordx4 v[238:241], v[250:251], off offset:256
	v_add_u32_e32 v250, 0xb0, v172
	v_ashrrev_i32_e32 v251, 31, v250
	v_lshlrev_b64 v[250:251], 11, v[250:251]
	v_lshl_add_u64 v[250:251], v[174:175], 0, v[250:251]
	global_load_dwordx4 v[242:245], v[250:251], off
	global_load_dwordx4 v[246:249], v[250:251], off offset:256
	v_lshl_add_u64 v[202:203], s[10:11], 0, v[202:203]
	v_lshl_add_u64 v[202:203], v[202:203], 0, s[30:31]
	s_lshl_b32 s26, s26, 2
	s_ashr_i32 s27, s26, 31
	s_waitcnt vmcnt(8)
	s_nop 0
	v_lshlrev_b32_e32 v204, 16, v194
	v_and_b32_e32 v194, 0xffff0000, v194
	v_lshlrev_b32_e32 v205, 16, v195
	v_and_b32_e32 v195, 0xffff0000, v195
	v_lshlrev_b32_e32 v206, 16, v196
	v_and_b32_e32 v196, 0xffff0000, v196
	v_lshlrev_b32_e32 v207, 16, v197
	v_and_b32_e32 v197, 0xffff0000, v197
	v_lshlrev_b32_e32 v208, 16, v198
	v_and_b32_e32 v198, 0xffff0000, v198
	v_lshlrev_b32_e32 v209, 16, v199
	v_and_b32_e32 v199, 0xffff0000, v199
	v_lshlrev_b32_e32 v210, 16, v200
	v_and_b32_e32 v200, 0xffff0000, v200
	v_add_f32_e32 v125, v125, v194
	v_add_f32_e32 v121, v121, v196
	v_add_f32_e32 v127, v127, v195
	v_add_f32_e32 v123, v123, v197
	v_add_f32_e32 v124, v124, v204
	v_add_f32_e32 v120, v120, v206
	v_add_f32_e32 v126, v126, v205
	v_add_f32_e32 v122, v122, v207
	v_add_f32_e32 v195, v112, v210
	v_add_f32_e32 v196, v117, v198
	v_add_f32_e32 v197, v113, v200
	v_add_f32_e32 v198, v118, v209
	v_add_f32_e32 v199, v119, v199
	v_mul_f32_e32 v112, v125, v125
	v_mul_f32_e32 v113, v127, v127
	v_mul_f32_e32 v118, v121, v121
	v_mul_f32_e32 v119, v123, v123
	v_lshlrev_b32_e32 v211, 16, v201
	v_and_b32_e32 v201, 0xffff0000, v201
	v_fmac_f32_e32 v112, v124, v124
	v_fmac_f32_e32 v113, v126, v126
	v_fmac_f32_e32 v118, v120, v120
	v_fmac_f32_e32 v119, v122, v122
	v_add_f32_e32 v201, v115, v201
	v_add_f32_e32 v112, v112, v113
	v_add_f32_e32 v113, v118, v119
	v_add_f32_e32 v194, v116, v208
	v_add_f32_e32 v200, v114, v211
	v_cvt_pk_bf16_f32 v114, v124, v125
	v_cvt_pk_bf16_f32 v115, v126, v127
	v_cvt_pk_bf16_f32 v116, v120, v121
	v_cvt_pk_bf16_f32 v117, v122, v123
	v_mul_f32_e32 v121, v196, v196
	v_mul_f32_e32 v123, v199, v199
	v_add_f32_e32 v112, v112, v113
	v_mul_f32_e32 v113, v197, v197
	v_mul_f32_e32 v119, v201, v201
	v_fmac_f32_e32 v121, v194, v194
	v_fmac_f32_e32 v123, v198, v198
	v_fmac_f32_e32 v113, v195, v195
	v_fmac_f32_e32 v119, v200, v200
	v_add_f32_e32 v118, v121, v123
	v_add_f32_e32 v113, v113, v119
	v_add_f32_e32 v113, v118, v113
	v_and_b32_e32 v118, 64, v193
	v_add_f32_e32 v113, v112, v113
	v_xor_b32_e32 v112, 16, v193
	v_add_u32_e32 v122, 64, v118
	v_cmp_lt_i32_e32 vcc, v112, v122
	v_lshl_add_u64 v[118:119], v[202:203], 0, s[6:7]
	v_lshl_add_u64 v[120:121], v[118:119], 0, v[160:161]
	v_cndmask_b32_e32 v112, v193, v112, vcc
	v_lshlrev_b32_e32 v112, 2, v112
	ds_bpermute_b32 v123, v112, v113
	global_store_dwordx4 v[120:121], v[114:117], off
	s_nop 1
	v_cvt_pk_bf16_f32 v116, v194, v196
	s_waitcnt lgkmcnt(0)
	v_add_f32_e32 v114, v113, v123
	v_xor_b32_e32 v113, 32, v193
	v_cmp_lt_i32_e32 vcc, v113, v122
	v_cvt_pk_bf16_f32 v117, v198, v199
	v_cvt_pk_bf16_f32 v118, v195, v197
	v_cvt_pk_bf16_f32 v119, v200, v201
	global_store_dwordx4 v[120:121], v[116:119], off offset:256
	s_nop 0
	v_cndmask_b32_e32 v113, v193, v113, vcc
	v_lshlrev_b32_e32 v113, 2, v113
	ds_bpermute_b32 v115, v113, v114
	s_and_saveexec_b64 s[30:31], s[2:3]
	s_cbranch_execz .LBB0_2730
	v_lshlrev_b64 v[116:117], 6, v[172:173]
	v_lshl_add_u64 v[116:117], s[12:13], 0, v[116:117]
	v_lshl_add_u64 v[116:117], s[26:27], 2, v[116:117]
	s_lshl_b32 s34, s44, 2
	s_mov_b32 s35, s7
	v_lshl_add_u64 v[116:117], v[116:117], 0, s[34:35]
	s_waitcnt lgkmcnt(0)
	v_add_f32_e32 v114, v114, v115
	global_store_dword v[116:117], v114, off

; __device__ __forceinline__ unsigned cvt_pk_bf16(float lo, float hi) { unsigned r; asm volatile("v_cvt_pk_bf16_f32 %0, %1, %2" : "=v"(r) : "v"(lo), "v"(hi)); return r; }
; __device__ __forceinline__ float dot4(f32x4 v) { return (v.x * v.x + v.y * v.y) + (v.z * v.z + v.w * v.w); }
;     __device__ __forceinline__ void operator()(const f32x4 (&acc)[2][2][4][2], const Unit& u, int wr, int wc, int fr, int fq) const {
;     ...
;             for (int m = 0; m < 4; ++m) {
;                 const int row = u.pm * BM + ai * HALF + wr * 64 + m * 16 + fr;
;                 float s = 0.f;
; #pragma unroll
;                 for (int bj = 0; bj < 2; ++bj) {
;                     const size_t off = (size_t)row * 1024 + u.pn * BM + bj * HALF + wc * 32 + 8 * fq;
;                     f32x4 r0, r1;
;                     if (RES_BF16) {
;                         const u32x4 w_ = rw[m][bj];
;                         r0 = (f32x4){__uint_as_float(w_.x << 16), __uint_as_float(w_.x & 0xffff0000u), __uint_as_float(w_.y << 16), __uint_as_float(w_.y & 0xffff0000u)};
;                         r1 = (f32x4){__uint_as_float(w_.z << 16), __uint_as_float(w_.z & 0xffff0000u), __uint_as_float(w_.w << 16), __uint_as_float(w_.w & 0xffff0000u)};
;                     } else { r0 = *(const f32x4*)(resid + off); r1 = *(const f32x4*)(resid + off + 4); }
;                     f32x4 v0, v1;
; #pragma unroll
;                     for (int j = 0; j < 4; ++j) { v0[j] = acc[ai][bj][m][0][j] + r0[j]; v1[j] = acc[ai][bj][m][1][j] + r1[j]; }
;                     if (OUT_F32) { *(f32x4*)(xout + off) = v0; *(f32x4*)(xout + off + 4) = v1; }
;                     else {
;                         u32x4 w; w.x = cvt_pk_bf16(v0[0], v0[1]); w.y = cvt_pk_bf16(v0[2], v0[3]); w.z = cvt_pk_bf16(v1[0], v1[1]); w.w = cvt_pk_bf16(v1[2], v1[3]);
;                         *(u32x4*)(xb + off) = w;
;                     }
;                     s += dot4(v0) + dot4(v1);
;                 }
;                 s += __shfl_xor(s, 16); s += __shfl_xor(s, 32);
;                 if (fq == 0) ssq[(size_t)row * 16 + u.pn * 4 + wc] = s;
.LBB0_2736:
	s_or_b64 exec, exec, s[30:31]
	v_add_u32_e32 v100, 0x80, v172
	v_ashrrev_i32_e32 v101, 31, v100
	v_add_u32_e32 v96, 0x90, v172
	v_lshlrev_b64 v[110:111], 11, v[100:101]
	v_ashrrev_i32_e32 v97, 31, v96
	v_add_u32_e32 v92, 0xa0, v172
	s_waitcnt lgkmcnt(0)
	v_lshlrev_b64 v[98:99], 11, v[96:97]
	v_ashrrev_i32_e32 v93, 31, v92
	v_add_u32_e32 v88, 0xb0, v172
	v_lshlrev_b64 v[94:95], 11, v[92:93]
	v_ashrrev_i32_e32 v89, 31, v88
	v_lshlrev_b64 v[90:91], 11, v[88:89]
	v_lshl_add_u64 v[110:111], s[10:11], 0, v[110:111]
	v_lshl_add_u64 v[110:111], s[28:29], 1, v[110:111]
	s_waitcnt vmcnt(8)
	v_lshlrev_b32_e32 v114, 16, v218
	v_and_b32_e32 v102, 0xffff0000, v218
	v_lshlrev_b32_e32 v115, 16, v219
	v_and_b32_e32 v103, 0xffff0000, v219
	v_lshlrev_b32_e32 v116, 16, v220
	v_and_b32_e32 v104, 0xffff0000, v220
	v_lshlrev_b32_e32 v117, 16, v221
	v_and_b32_e32 v105, 0xffff0000, v221
	v_lshlrev_b32_e32 v118, 16, v222
	v_and_b32_e32 v106, 0xffff0000, v222
	v_lshlrev_b32_e32 v119, 16, v223
	v_and_b32_e32 v107, 0xffff0000, v223
	v_lshlrev_b32_e32 v120, 16, v224
	v_and_b32_e32 v108, 0xffff0000, v224
	v_lshlrev_b32_e32 v121, 16, v225
	v_and_b32_e32 v109, 0xffff0000, v225
	v_add_f32_e32 v61, v61, v102
	v_add_f32_e32 v57, v57, v104
	v_add_f32_e32 v63, v63, v103
	v_add_f32_e32 v59, v59, v105
	v_add_f32_e32 v104, v53, v106
	v_add_f32_e32 v105, v49, v108
	v_add_f32_e32 v107, v55, v107
	v_add_f32_e32 v109, v51, v109
	v_add_f32_e32 v60, v60, v114
	v_add_f32_e32 v56, v56, v116
	v_add_f32_e32 v62, v62, v115
	v_add_f32_e32 v58, v58, v117
	v_add_f32_e32 v102, v52, v118
	v_add_f32_e32 v103, v48, v120
	v_add_f32_e32 v106, v54, v119
	v_add_f32_e32 v108, v50, v121
	v_cvt_pk_bf16_f32 v48, v60, v61
	v_cvt_pk_bf16_f32 v49, v62, v63
	v_cvt_pk_bf16_f32 v50, v56, v57
	v_cvt_pk_bf16_f32 v51, v58, v59
	v_mul_f32_e32 v52, v61, v61
	v_mul_f32_e32 v53, v63, v63
	v_mul_f32_e32 v54, v57, v57
	v_mul_f32_e32 v55, v59, v59
	v_mul_f32_e32 v57, v104, v104
	v_mul_f32_e32 v59, v107, v107
	v_mul_f32_e32 v61, v105, v105
	v_mul_f32_e32 v63, v109, v109
	v_fmac_f32_e32 v52, v60, v60
	v_fmac_f32_e32 v53, v62, v62
	v_fmac_f32_e32 v54, v56, v56
	v_fmac_f32_e32 v55, v58, v58
	v_fmac_f32_e32 v57, v102, v102
	v_fmac_f32_e32 v59, v106, v106
	v_fmac_f32_e32 v61, v103, v103
	v_fmac_f32_e32 v63, v108, v108
	v_add_f32_e32 v52, v52, v53
	v_add_f32_e32 v53, v54, v55
	v_add_f32_e32 v54, v57, v59
	v_add_f32_e32 v55, v61, v63
	v_add_f32_e32 v52, v52, v53
	v_add_f32_e32 v53, v54, v55
	v_add_f32_e32 v56, v52, v53
	ds_bpermute_b32 v57, v112, v56
	v_lshl_add_u64 v[52:53], v[110:111], 0, s[6:7]
	v_lshl_add_u64 v[54:55], v[52:53], 0, v[160:161]
	global_store_dwordx4 v[54:55], v[48:51], off
	s_waitcnt lgkmcnt(0)
	s_nop 0
	v_add_f32_e32 v48, v56, v57
	ds_bpermute_b32 v49, v113, v48
	v_cvt_pk_bf16_f32 v50, v102, v104
	v_cvt_pk_bf16_f32 v51, v106, v107
	v_cvt_pk_bf16_f32 v52, v103, v105
	v_cvt_pk_bf16_f32 v53, v108, v109
	global_store_dwordx4 v[54:55], v[50:53], off offset:256
	s_and_saveexec_b64 s[30:31], s[2:3]
	s_cbranch_execz .LBB0_2738
	v_lshlrev_b64 v[50:51], 6, v[100:101]
	v_lshl_add_u64 v[50:51], s[12:13], 0, v[50:51]
	v_lshl_add_u64 v[50:51], s[26:27], 2, v[50:51]
	s_lshl_b32 s34, s44, 2
	s_mov_b32 s35, s7
	v_lshl_add_u64 v[50:51], v[50:51], 0, s[34:35]
	s_waitcnt lgkmcnt(0)
	v_add_f32_e32 v48, v48, v49
	global_store_dword v[50:51], v48, off
.LBB0_2738:
	s_or_b64 exec, exec, s[30:31]
	s_waitcnt lgkmcnt(0)
	v_and_b32_e32 v49, 0xffff0000, v226
	v_and_b32_e32 v51, 0xffff0000, v227
	v_lshlrev_b32_e32 v48, 16, v226
	v_lshlrev_b32_e32 v50, 16, v227
	v_lshlrev_b32_e32 v52, 16, v228
	v_and_b32_e32 v53, 0xffff0000, v228
	v_add_f32_e32 v49, v45, v49
	v_add_f32_e32 v47, v47, v51
	v_and_b32_e32 v55, 0xffff0000, v229
	v_add_f32_e32 v48, v44, v48
	v_add_f32_e32 v52, v40, v52
	v_add_f32_e32 v53, v41, v53
	v_add_f32_e32 v46, v46, v50
	v_cvt_pk_bf16_f32 v40, v48, v49
	v_cvt_pk_bf16_f32 v41, v46, v47
	v_mul_f32_e32 v49, v49, v49
	v_mul_f32_e32 v47, v47, v47
	v_lshlrev_b32_e32 v54, 16, v229
	v_add_f32_e32 v51, v43, v55
	v_fmac_f32_e32 v49, v48, v48
	v_fmac_f32_e32 v47, v46, v46
	v_add_f32_e32 v50, v42, v54
	v_add_f32_e32 v46, v49, v47
	v_mul_f32_e32 v47, v53, v53
	v_mul_f32_e32 v48, v51, v51
	v_fmac_f32_e32 v47, v52, v52
	v_fmac_f32_e32 v48, v50, v50
	v_cvt_pk_bf16_f32 v42, v52, v53
	v_cvt_pk_bf16_f32 v43, v50, v51
	v_add_f32_e32 v47, v47, v48
	v_and_b32_e32 v48, 0xffff0000, v230
	v_and_b32_e32 v50, 0xffff0000, v231
	v_add_f32_e32 v46, v46, v47
	v_lshlrev_b32_e32 v47, 16, v230
	v_lshlrev_b32_e32 v49, 16, v231
	v_lshlrev_b32_e32 v51, 16, v232
	v_and_b32_e32 v52, 0xffff0000, v232
	v_add_f32_e32 v37, v37, v48
	v_add_f32_e32 v50, v39, v50
	v_and_b32_e32 v54, 0xffff0000, v233
	v_add_f32_e32 v36, v36, v47
	v_add_f32_e32 v47, v32, v51
	v_add_f32_e32 v48, v33, v52
	v_add_f32_e32 v49, v38, v49
	v_mul_f32_e32 v32, v37, v37
	v_mul_f32_e32 v33, v50, v50
	v_lshlrev_b32_e32 v53, 16, v233
	v_add_f32_e32 v52, v35, v54
	v_fmac_f32_e32 v32, v36, v36
	v_fmac_f32_e32 v33, v49, v49
	v_add_f32_e32 v51, v34, v53
	v_add_f32_e32 v32, v32, v33
	v_mul_f32_e32 v33, v48, v48
	v_mul_f32_e32 v34, v52, v52
	v_fmac_f32_e32 v33, v47, v47
	v_fmac_f32_e32 v34, v51, v51
	v_add_f32_e32 v33, v33, v34
	v_add_f32_e32 v32, v32, v33
	v_add_f32_e32 v35, v46, v32
	ds_bpermute_b32 v46, v112, v35
	v_lshl_add_u64 v[44:45], s[10:11], 0, v[98:99]
	v_lshl_add_u64 v[44:45], s[28:29], 1, v[44:45]
	v_lshl_add_u64 v[32:33], v[44:45], 0, s[6:7]
	v_lshl_add_u64 v[38:39], v[32:33], 0, v[160:161]
	s_waitcnt lgkmcnt(0)
	v_add_f32_e32 v32, v35, v46
	ds_bpermute_b32 v33, v113, v32
	global_store_dwordx4 v[38:39], v[40:43], off
	v_cvt_pk_bf16_f32 v34, v36, v37
	v_cvt_pk_bf16_f32 v35, v49, v50
	v_cvt_pk_bf16_f32 v36, v47, v48
	v_cvt_pk_bf16_f32 v37, v51, v52
	global_store_dwordx4 v[38:39], v[34:37], off offset:256
	s_and_saveexec_b64 s[30:31], s[2:3]
	s_cbranch_execz .LBB0_2740
	v_lshlrev_b64 v[34:35], 6, v[96:97]
	v_lshl_add_u64 v[34:35], s[12:13], 0, v[34:35]
	v_lshl_add_u64 v[34:35], s[26:27], 2, v[34:35]
	s_lshl_b32 s34, s44, 2
	s_mov_b32 s35, s7
	v_lshl_add_u64 v[34:35], v[34:35], 0, s[34:35]
	s_waitcnt lgkmcnt(0)
	v_add_f32_e32 v32, v32, v33
	global_store_dword v[34:35], v32, off
; __device__ __forceinline__ unsigned cvt_pk_bf16(float lo, float hi) { unsigned r; asm volatile("v_cvt_pk_bf16_f32 %0, %1, %2" : "=v"(r) : "v"(lo), "v"(hi)); return r; }
; __device__ __forceinline__ float dot4(f32x4 v) { return (v.x * v.x + v.y * v.y) + (v.z * v.z + v.w * v.w); }
;     __device__ __forceinline__ void operator()(const f32x4 (&acc)[2][2][4][2], const Unit& u, int wr, int wc, int fr, int fq) const {
;     ...
;             for (int m = 0; m < 4; ++m) {
;                 const int row = u.pm * BM + ai * HALF + wr * 64 + m * 16 + fr;
;                 float s = 0.f;
; #pragma unroll
;                 for (int bj = 0; bj < 2; ++bj) {
;                     const size_t off = (size_t)row * 1024 + u.pn * BM + bj * HALF + wc * 32 + 8 * fq;
;                     f32x4 r0, r1;
;                     if (RES_BF16) {
;                         const u32x4 w_ = rw[m][bj];
;                         r0 = (f32x4){__uint_as_float(w_.x << 16), __uint_as_float(w_.x & 0xffff0000u), __uint_as_float(w_.y << 16), __uint_as_float(w_.y & 0xffff0000u)};
;                         r1 = (f32x4){__uint_as_float(w_.z << 16), __uint_as_float(w_.z & 0xffff0000u), __uint_as_float(w_.w << 16), __uint_as_float(w_.w & 0xffff0000u)};
;                     } else { r0 = *(const f32x4*)(resid + off); r1 = *(const f32x4*)(resid + off + 4); }
;                     f32x4 v0, v1;
; #pragma unroll
;                     for (int j = 0; j < 4; ++j) { v0[j] = acc[ai][bj][m][0][j] + r0[j]; v1[j] = acc[ai][bj][m][1][j] + r1[j]; }
;                     if (OUT_F32) { *(f32x4*)(xout + off) = v0; *(f32x4*)(xout + off + 4) = v1; }
;                     else {
;                         u32x4 w; w.x = cvt_pk_bf16(v0[0], v0[1]); w.y = cvt_pk_bf16(v0[2], v0[3]); w.z = cvt_pk_bf16(v1[0], v1[1]); w.w = cvt_pk_bf16(v1[2], v1[3]);
;                         *(u32x4*)(xb + off) = w;
;                     }
;                     s += dot4(v0) + dot4(v1);
;                 }
;                 s += __shfl_xor(s, 16); s += __shfl_xor(s, 32);
;                 if (fq == 0) ssq[(size_t)row * 16 + u.pn * 4 + wc] = s;
.LBB0_2740:
	s_or_b64 exec, exec, s[30:31]
	s_waitcnt lgkmcnt(0)
	v_and_b32_e32 v33, 0xffff0000, v234
	v_and_b32_e32 v35, 0xffff0000, v235
	v_lshlrev_b32_e32 v32, 16, v234
	v_lshlrev_b32_e32 v34, 16, v235
	v_lshlrev_b32_e32 v36, 16, v236
	v_and_b32_e32 v37, 0xffff0000, v236
	v_add_f32_e32 v33, v29, v33
	v_add_f32_e32 v31, v31, v35
	v_and_b32_e32 v39, 0xffff0000, v237
	v_add_f32_e32 v32, v28, v32
	v_add_f32_e32 v36, v24, v36
	v_add_f32_e32 v37, v25, v37
	v_add_f32_e32 v30, v30, v34
	v_cvt_pk_bf16_f32 v24, v32, v33
	v_cvt_pk_bf16_f32 v25, v30, v31
	v_mul_f32_e32 v33, v33, v33
	v_mul_f32_e32 v31, v31, v31
	v_lshlrev_b32_e32 v38, 16, v237
	v_add_f32_e32 v35, v27, v39
	v_fmac_f32_e32 v33, v32, v32
	v_fmac_f32_e32 v31, v30, v30
	v_add_f32_e32 v34, v26, v38
	v_add_f32_e32 v30, v33, v31
	v_mul_f32_e32 v31, v37, v37
	v_mul_f32_e32 v32, v35, v35
	v_fmac_f32_e32 v31, v36, v36
	v_fmac_f32_e32 v32, v34, v34
	v_cvt_pk_bf16_f32 v26, v36, v37
	v_cvt_pk_bf16_f32 v27, v34, v35
	v_add_f32_e32 v31, v31, v32
	v_and_b32_e32 v32, 0xffff0000, v238
	v_and_b32_e32 v34, 0xffff0000, v239
	v_add_f32_e32 v30, v30, v31
	v_lshlrev_b32_e32 v31, 16, v238
	v_lshlrev_b32_e32 v33, 16, v239
	v_lshlrev_b32_e32 v35, 16, v240
	v_and_b32_e32 v36, 0xffff0000, v240
	v_add_f32_e32 v21, v21, v32
	v_add_f32_e32 v34, v23, v34
	v_and_b32_e32 v38, 0xffff0000, v241
	v_add_f32_e32 v20, v20, v31
	v_add_f32_e32 v31, v16, v35
	v_add_f32_e32 v32, v17, v36
	v_add_f32_e32 v33, v22, v33
	v_mul_f32_e32 v16, v21, v21
	v_mul_f32_e32 v17, v34, v34
	v_lshlrev_b32_e32 v37, 16, v241
	v_add_f32_e32 v36, v19, v38
	v_fmac_f32_e32 v16, v20, v20
	v_fmac_f32_e32 v17, v33, v33
	v_add_f32_e32 v35, v18, v37
	v_add_f32_e32 v16, v16, v17
	v_mul_f32_e32 v17, v32, v32
	v_mul_f32_e32 v18, v36, v36
	v_fmac_f32_e32 v17, v31, v31
	v_fmac_f32_e32 v18, v35, v35
	v_add_f32_e32 v17, v17, v18
	v_add_f32_e32 v16, v16, v17
	v_add_f32_e32 v19, v30, v16
	ds_bpermute_b32 v30, v112, v19
	v_lshl_add_u64 v[28:29], s[10:11], 0, v[94:95]
	v_lshl_add_u64 v[28:29], s[28:29], 1, v[28:29]
	v_lshl_add_u64 v[16:17], v[28:29], 0, s[6:7]
	v_lshl_add_u64 v[22:23], v[16:17], 0, v[160:161]
	s_waitcnt lgkmcnt(0)
	v_add_f32_e32 v16, v19, v30
	ds_bpermute_b32 v17, v113, v16
	global_store_dwordx4 v[22:23], v[24:27], off
	v_cvt_pk_bf16_f32 v18, v20, v21
	v_cvt_pk_bf16_f32 v19, v33, v34
	v_cvt_pk_bf16_f32 v20, v31, v32
	v_cvt_pk_bf16_f32 v21, v35, v36
	global_store_dwordx4 v[22:23], v[18:21], off offset:256
	s_and_saveexec_b64 s[30:31], s[2:3]
	s_cbranch_execz .LBB0_2742
	v_lshlrev_b64 v[18:19], 6, v[92:93]
	v_lshl_add_u64 v[18:19], s[12:13], 0, v[18:19]
	v_lshl_add_u64 v[18:19], s[26:27], 2, v[18:19]
	s_lshl_b32 s34, s44, 2
	s_mov_b32 s35, s7
	v_lshl_add_u64 v[18:19], v[18:19], 0, s[34:35]
	s_waitcnt lgkmcnt(0)
	v_add_f32_e32 v16, v16, v17
	global_store_dword v[18:19], v16, off
.LBB0_2742:
	s_or_b64 exec, exec, s[30:31]
	s_waitcnt lgkmcnt(0)
	v_and_b32_e32 v17, 0xffff0000, v242
	v_and_b32_e32 v19, 0xffff0000, v243
	v_lshlrev_b32_e32 v16, 16, v242
	v_lshlrev_b32_e32 v18, 16, v243
	v_lshlrev_b32_e32 v20, 16, v244
	v_and_b32_e32 v21, 0xffff0000, v244
	v_add_f32_e32 v17, v13, v17
	v_add_f32_e32 v15, v15, v19
	v_and_b32_e32 v23, 0xffff0000, v245
	v_add_f32_e32 v16, v12, v16
	v_add_f32_e32 v20, v8, v20
	v_add_f32_e32 v21, v9, v21
	v_add_f32_e32 v14, v14, v18
	v_cvt_pk_bf16_f32 v8, v16, v17
	v_cvt_pk_bf16_f32 v9, v14, v15
	v_mul_f32_e32 v17, v17, v17
	v_mul_f32_e32 v15, v15, v15
	v_lshlrev_b32_e32 v22, 16, v245
	v_add_f32_e32 v19, v11, v23
	v_fmac_f32_e32 v17, v16, v16
	v_fmac_f32_e32 v15, v14, v14
	v_add_f32_e32 v18, v10, v22
	v_add_f32_e32 v14, v17, v15
	v_mul_f32_e32 v15, v21, v21
	v_mul_f32_e32 v16, v19, v19
	v_fmac_f32_e32 v15, v20, v20
	v_fmac_f32_e32 v16, v18, v18
	v_cvt_pk_bf16_f32 v10, v20, v21
	v_cvt_pk_bf16_f32 v11, v18, v19
	v_add_f32_e32 v15, v15, v16
	v_and_b32_e32 v16, 0xffff0000, v246
	v_and_b32_e32 v18, 0xffff0000, v247
	v_add_f32_e32 v14, v14, v15
	v_lshlrev_b32_e32 v15, 16, v246
	v_lshlrev_b32_e32 v17, 16, v247
	v_lshlrev_b32_e32 v19, 16, v248
	v_and_b32_e32 v20, 0xffff0000, v248
	v_add_f32_e32 v5, v5, v16
	v_add_f32_e32 v18, v7, v18
	v_and_b32_e32 v22, 0xffff0000, v249
	v_add_f32_e32 v4, v4, v15
	v_add_f32_e32 v15, v0, v19
	v_add_f32_e32 v16, v1, v20
	v_add_f32_e32 v17, v6, v17
	v_mul_f32_e32 v0, v5, v5
	v_mul_f32_e32 v1, v18, v18
	v_lshlrev_b32_e32 v21, 16, v249
	v_add_f32_e32 v20, v3, v22
	v_fmac_f32_e32 v0, v4, v4
	v_fmac_f32_e32 v1, v17, v17
	v_add_f32_e32 v19, v2, v21
	v_add_f32_e32 v0, v0, v1
	v_mul_f32_e32 v1, v16, v16
	v_mul_f32_e32 v2, v20, v20
	v_fmac_f32_e32 v1, v15, v15
	v_fmac_f32_e32 v2, v19, v19
	v_add_f32_e32 v1, v1, v2
	v_add_f32_e32 v0, v0, v1
	v_add_f32_e32 v3, v14, v0
	ds_bpermute_b32 v14, v112, v3
	v_lshl_add_u64 v[12:13], s[10:11], 0, v[90:91]
	v_lshl_add_u64 v[12:13], s[28:29], 1, v[12:13]
	v_lshl_add_u64 v[0:1], v[12:13], 0, s[6:7]
	v_lshl_add_u64 v[6:7], v[0:1], 0, v[160:161]
	s_waitcnt lgkmcnt(0)
	v_add_f32_e32 v0, v3, v14
	ds_bpermute_b32 v1, v113, v0
	global_store_dwordx4 v[6:7], v[8:11], off
	v_cvt_pk_bf16_f32 v2, v4, v5
	v_cvt_pk_bf16_f32 v3, v17, v18
	v_cvt_pk_bf16_f32 v4, v15, v16
	v_cvt_pk_bf16_f32 v5, v19, v20
	global_store_dwordx4 v[6:7], v[2:5], off offset:256
	s_and_saveexec_b64 s[28:29], s[2:3]
	s_cbranch_execz .LBB0_2744
	v_lshlrev_b64 v[2:3], 6, v[88:89]
	v_lshl_add_u64 v[2:3], s[12:13], 0, v[2:3]
	v_lshl_add_u64 v[2:3], s[26:27], 2, v[2:3]
	s_lshl_b32 s26, s44, 2
	s_mov_b32 s27, s7
	v_lshl_add_u64 v[2:3], v[2:3], 0, s[26:27]
	s_waitcnt lgkmcnt(0)
	v_add_f32_e32 v0, v0, v1
	global_store_dword v[2:3], v0, off

;     __device__ __forceinline__ void operator()(const f32x4 (&acc)[2][2][4][2], const Unit& u, int wr, int wc, int fr, int fq) const {
;     ...
;             if (RES_BF16) {
; #pragma unroll
;                 for (int m = 0; m < 4; ++m)
; #pragma unroll
;                     for (int bj = 0; bj < 2; ++bj)
;                         rw[m][bj] = *(const u32x4*)(xb + (size_t)(u.pm * BM + ai * HALF + wr * 64 + m * 16 + fr) * 1024 + u.pn * BM + bj * HALF + wc * 32 + 8 * fq);
; #pragma unroll
;                 for (int m = 0; m < 4; ++m)
; #pragma unroll
;                     for (int bj = 0; bj < 2; ++bj) asm volatile("" : "+v"(rw[m][bj]));
;             }
; #pragma unroll
;             for (int m = 0; m < 4; ++m) {
;                 const int row = u.pm * BM + ai * HALF + wr * 64 + m * 16 + fr;
;                 float s = 0.f;
; #pragma unroll
;                 for (int bj = 0; bj < 2; ++bj) {
;                     const size_t off = (size_t)row * 1024 + u.pn * BM + bj * HALF + wc * 32 + 8 * fq;
;                     f32x4 r0, r1;
;                     if (RES_BF16) {
;                         const u32x4 w_ = rw[m][bj];
;                         r0 = (f32x4){__uint_as_float(w_.x << 16), __uint_as_float(w_.x & 0xffff0000u), __uint_as_float(w_.y << 16), __uint_as_float(w_.y & 0xffff0000u)};
;                         r1 = (f32x4){__uint_as_float(w_.z << 16), __uint_as_float(w_.z & 0xffff0000u), __uint_as_float(w_.w << 16), __uint_as_float(w_.w & 0xffff0000u)};
;                     } else { r0 = *(const f32x4*)(resid + off); r1 = *(const f32x4*)(resid + off + 4); }
;                     f32x4 v0, v1;
; #pragma unroll
;                     for (int j = 0; j < 4; ++j) { v0[j] = acc[ai][bj][m][0][j] + r0[j]; v1[j] = acc[ai][bj][m][1][j] + r1[j]; }
;                     if (OUT_F32) { *(f32x4*)(xout + off) = v0; *(f32x4*)(xout + off + 4) = v1; }
;                     else {
;                         u32x4 w; w.x = cvt_pk_bf16(v0[0], v0[1]); w.y = cvt_pk_bf16(v0[2], v0[3]); w.z = cvt_pk_bf16(v1[0], v1[1]); w.w = cvt_pk_bf16(v1[2], v1[3]);
;                         *(u32x4*)(xb + off) = w;
;                     }
;                     s += dot4(v0) + dot4(v1);
;                 }
;                 s += __shfl_xor(s, 16); s += __shfl_xor(s, 32);
;                 if (fq == 0) ssq[(size_t)row * 16 + u.pn * 4 + wc] = s;
.LBB0_2900:
	s_lshl_b32 s24, s48, 8
	v_lshl_add_u32 v172, s49, 8, v188
	s_ashr_i32 s25, s24, 31
	s_lshl_b64 s[26:27], s[24:25], 1
	v_ashrrev_i32_e32 v173, 31, v172
	v_lshl_add_u64 v[174:175], v[162:163], 0, s[26:27]
	v_lshlrev_b64 v[202:203], 11, v[172:173]
	v_lshl_add_u64 v[128:129], v[174:175], 0, v[202:203]
	v_or_b32_e32 v184, 16, v172
	global_load_dwordx4 v[194:197], v[128:129], off
	global_load_dwordx4 v[198:201], v[128:129], off offset:256
	v_ashrrev_i32_e32 v185, 31, v184
	v_or_b32_e32 v180, 32, v172
	v_lshlrev_b64 v[186:187], 11, v[184:185]
	v_ashrrev_i32_e32 v181, 31, v180
	v_or_b32_e32 v176, 48, v172
	v_lshl_add_u64 v[128:129], v[174:175], 0, v[186:187]
	v_lshlrev_b64 v[182:183], 11, v[180:181]
	v_ashrrev_i32_e32 v177, 31, v176
	global_load_dwordx4 v[148:151], v[128:129], off
	global_load_dwordx4 v[144:147], v[128:129], off offset:256
	v_lshl_add_u64 v[128:129], v[174:175], 0, v[182:183]
	v_lshlrev_b64 v[178:179], 11, v[176:177]
	global_load_dwordx4 v[140:143], v[128:129], off
	global_load_dwordx4 v[136:139], v[128:129], off offset:256
	v_lshl_add_u64 v[128:129], v[174:175], 0, v[178:179]
	global_load_dwordx4 v[132:135], v[128:129], off
	s_nop 0
	global_load_dwordx4 v[128:131], v[128:129], off offset:256
	v_add_u32_e32 v250, 0x80, v172
	v_ashrrev_i32_e32 v251, 31, v250
	v_lshlrev_b64 v[250:251], 11, v[250:251]
	v_lshl_add_u64 v[250:251], v[174:175], 0, v[250:251]
	global_load_dwordx4 v[218:221], v[250:251], off
	global_load_dwordx4 v[222:225], v[250:251], off offset:256
	v_add_u32_e32 v250, 0x90, v172
	v_ashrrev_i32_e32 v251, 31, v250
	v_lshlrev_b64 v[250:251], 11, v[250:251]
	v_lshl_add_u64 v[250:251], v[174:175], 0, v[250:251]
	global_load_dwordx4 v[226:229], v[250:251], off
	global_load_dwordx4 v[230:233], v[250:251], off offset:256
	v_add_u32_e32 v250, 0xa0, v172
	v_ashrrev_i32_e32 v251, 31, v250
	v_lshlrev_b64 v[250:251], 11, v[250:251]
	v_lshl_add_u64 v[250:251], v[174:175], 0, v[250:251]
	global_load_dwordx4 v[234:237], v[250:251], off
	global_load_dwordx4 v[238:241], v[250:251], off offset:256
	v_add_u32_e32 v250, 0xb0, v172
	v_ashrrev_i32_e32 v251, 31, v250
	v_lshlrev_b64 v[250:251], 11, v[250:251]
	v_lshl_add_u64 v[250:251], v[174:175], 0, v[250:251]
	global_load_dwordx4 v[242:245], v[250:251], off
	global_load_dwordx4 v[246:249], v[250:251], off offset:256
	v_lshl_add_u64 v[202:203], s[12:13], 0, v[202:203]
	v_lshl_add_u64 v[202:203], v[202:203], 0, s[26:27]
	s_lshl_b32 s22, s48, 2
	s_ashr_i32 s23, s22, 31
	s_waitcnt vmcnt(8)
	s_nop 0
	v_lshlrev_b32_e32 v204, 16, v194
	v_and_b32_e32 v194, 0xffff0000, v194
	v_lshlrev_b32_e32 v205, 16, v195
	v_and_b32_e32 v195, 0xffff0000, v195
	v_lshlrev_b32_e32 v206, 16, v196
	v_and_b32_e32 v196, 0xffff0000, v196
	v_lshlrev_b32_e32 v207, 16, v197
	v_and_b32_e32 v197, 0xffff0000, v197
	v_lshlrev_b32_e32 v208, 16, v198
	v_and_b32_e32 v198, 0xffff0000, v198
	v_lshlrev_b32_e32 v209, 16, v199
	v_and_b32_e32 v199, 0xffff0000, v199
	v_lshlrev_b32_e32 v210, 16, v200
	v_and_b32_e32 v200, 0xffff0000, v200
	v_add_f32_e32 v125, v125, v194
	v_add_f32_e32 v121, v121, v196
	v_add_f32_e32 v127, v127, v195
	v_add_f32_e32 v123, v123, v197
	v_add_f32_e32 v124, v124, v204
	v_add_f32_e32 v120, v120, v206
	v_add_f32_e32 v126, v126, v205
	v_add_f32_e32 v122, v122, v207
	v_add_f32_e32 v195, v112, v210
	v_add_f32_e32 v196, v117, v198
	v_add_f32_e32 v197, v113, v200
	v_add_f32_e32 v198, v118, v209
	v_add_f32_e32 v199, v119, v199
	v_mul_f32_e32 v112, v125, v125
	v_mul_f32_e32 v113, v127, v127
	v_mul_f32_e32 v118, v121, v121
	v_mul_f32_e32 v119, v123, v123
	v_lshlrev_b32_e32 v211, 16, v201
	v_and_b32_e32 v201, 0xffff0000, v201
	v_fmac_f32_e32 v112, v124, v124
	v_fmac_f32_e32 v113, v126, v126
	v_fmac_f32_e32 v118, v120, v120
	v_fmac_f32_e32 v119, v122, v122
	v_add_f32_e32 v201, v115, v201
	v_add_f32_e32 v112, v112, v113
	v_add_f32_e32 v113, v118, v119
	v_add_f32_e32 v194, v116, v208
	v_add_f32_e32 v200, v114, v211
	v_cvt_pk_bf16_f32 v114, v124, v125
	v_cvt_pk_bf16_f32 v115, v126, v127
	v_cvt_pk_bf16_f32 v116, v120, v121
	v_cvt_pk_bf16_f32 v117, v122, v123
	v_mul_f32_e32 v121, v196, v196
	v_mul_f32_e32 v123, v199, v199
	v_add_f32_e32 v112, v112, v113
	v_mul_f32_e32 v113, v197, v197
	v_mul_f32_e32 v119, v201, v201
	v_fmac_f32_e32 v121, v194, v194
	v_fmac_f32_e32 v123, v198, v198
	v_fmac_f32_e32 v113, v195, v195
	v_fmac_f32_e32 v119, v200, v200
	v_add_f32_e32 v118, v121, v123
	v_add_f32_e32 v113, v113, v119
	v_add_f32_e32 v113, v118, v113
	v_and_b32_e32 v118, 64, v193
	v_add_f32_e32 v113, v112, v113
	v_xor_b32_e32 v112, 16, v193
	v_add_u32_e32 v122, 64, v118
	v_cmp_lt_i32_e32 vcc, v112, v122
	v_lshl_add_u64 v[118:119], v[202:203], 0, s[8:9]
	v_lshl_add_u64 v[120:121], v[118:119], 0, v[160:161]
	v_cndmask_b32_e32 v112, v193, v112, vcc
	v_lshlrev_b32_e32 v112, 2, v112
	ds_bpermute_b32 v123, v112, v113
	global_store_dwordx4 v[120:121], v[114:117], off
	s_nop 1
	v_cvt_pk_bf16_f32 v116, v194, v196
	s_waitcnt lgkmcnt(0)
	v_add_f32_e32 v114, v113, v123
	v_xor_b32_e32 v113, 32, v193
	v_cmp_lt_i32_e32 vcc, v113, v122
	v_cvt_pk_bf16_f32 v117, v198, v199
	v_cvt_pk_bf16_f32 v118, v195, v197
	v_cvt_pk_bf16_f32 v119, v200, v201
	global_store_dwordx4 v[120:121], v[116:119], off offset:256
	s_nop 0
	v_cndmask_b32_e32 v113, v193, v113, vcc
	v_lshlrev_b32_e32 v113, 2, v113
	ds_bpermute_b32 v115, v113, v114
	s_and_saveexec_b64 s[26:27], s[2:3]
	s_cbranch_execz .LBB0_2902
	v_lshlrev_b64 v[116:117], 6, v[172:173]
	v_lshl_add_u64 v[116:117], s[14:15], 0, v[116:117]
	v_lshl_add_u64 v[116:117], s[22:23], 2, v[116:117]
	s_lshl_b32 s28, s38, 2
	s_mov_b32 s29, s9
	v_lshl_add_u64 v[116:117], v[116:117], 0, s[28:29]
	s_waitcnt lgkmcnt(0)
	v_add_f32_e32 v114, v114, v115
	global_store_dword v[116:117], v114, off
